# adds router logits: the 16 x-fragment loads of a wave issued together (was load, vmcnt(0), 2 MFMAs, 16 times in a row)
# speedup vs baseline: 1.0196x; 1.0022x over previous
.LBB0_1741:
	s_mov_b32 s72, s73
	v_readlane_b32 s2, v254, 4
	v_readlane_b32 s1, v254, 2
	s_mov_b32 s4, 2
	v_readlane_b32 s1, v254, 3
	v_readlane_b32 s0, v255, 4
	s_ashr_i32 s5, s4, 31
	s_lshl_b32 s0, s0, 10
	s_lshl_b64 s[4:5], s[4:5], 3
	s_add_u32 s4, s94, s4
	s_addc_u32 s5, s95, s5
	s_load_dwordx2 s[4:5], s[4:5], 0x0
	s_mov_b32 s1, s73
	s_lshl_b64 s[76:77], s[0:1], 2
	s_mov_b32 s0, 18
	s_waitcnt lgkmcnt(0)
	s_add_u32 s4, s4, s76
	s_addc_u32 s5, s5, s77
	s_ashr_i32 s1, s0, 31
	s_lshl_b64 s[0:1], s[0:1], 3
	s_add_u32 s0, s94, s0
	s_addc_u32 s1, s95, s1
	s_load_dwordx2 s[8:9], s[0:1], 0x0
	s_mov_b32 s0, 19
	v_mov_b32_e32 v19, v0
	s_ashr_i32 s1, s0, 31
	v_and_b32_e32 v112, 63, v19
	v_lshlrev_b32_e32 v1, 6, v112
	global_load_dwordx4 v[4:7], v1, s[4:5] offset:48
	global_load_dwordx4 v[8:11], v1, s[4:5] offset:32
	global_load_dwordx4 v[12:15], v1, s[4:5] offset:16
	global_load_dwordx4 v[36:39], v1, s[4:5]
	s_lshl_b64 s[0:1], s[0:1], 3
	s_add_u32 s0, s94, s0
	s_addc_u32 s1, s95, s1
	v_readfirstlane_b32 s3, v19
	v_cmp_gt_i32_e64 s[6:7], 32, v19
	v_lshl_add_u32 v113, v19, 2, 0
	s_and_saveexec_b64 s[10:11], s[6:7]
	v_add_u32_e32 v1, 0x22500, v113
	ds_write_b32 v1, v3
	s_or_b64 exec, exec, s[10:11]
	v_readlane_b32 s10, v255, 4
	v_readlane_b32 s12, v254, 15
	s_lshl_b32 s10, s10, 15
	v_readlane_b32 s14, v254, 17
	s_mov_b32 s11, s73
	v_readlane_b32 s15, v254, 18
	s_add_u32 s80, s14, s72
	s_addc_u32 s81, s15, 0
	s_lshl_b64 s[10:11], s[10:11], 2
	s_waitcnt lgkmcnt(0)
	s_add_u32 s8, s8, s10
	s_addc_u32 s9, s9, s11
	s_ashr_i32 s89, s3, 6
	v_lshrrev_b32_e32 v1, 5, v112
	s_lshl_b32 s78, s89, 7
	v_lshl_or_b32 v30, v1, 3, s78
	v_and_b32_e32 v114, 31, v19
	v_or_b32_e32 v34, 1, v30
	v_lshlrev_b32_e32 v2, 2, v114
	v_ashrrev_i32_e32 v31, 31, v30
	v_ashrrev_i32_e32 v35, 31, v34
	v_lshl_add_u64 v[28:29], s[8:9], 0, v[2:3]
	s_waitcnt vmcnt(4)
	v_lshlrev_b64 v[20:21], 7, v[30:31]
	v_lshlrev_b64 v[34:35], 7, v[34:35]
	v_lshl_add_u64 v[20:21], v[28:29], 0, v[20:21]
	v_lshl_add_u64 v[32:33], v[30:31], 2, s[4:5]
	v_lshl_add_u64 v[34:35], v[28:29], 0, v[34:35]
	s_load_dwordx2 s[0:1], s[0:1], 0x0
	v_lshlrev_b32_e32 v108, 4, v1
	global_load_dword v1, v[20:21], off
	s_nop 0
	global_load_dwordx4 v[20:23], v[32:33], off offset:16
	global_load_dwordx4 v[24:27], v[32:33], off
	global_load_dword v41, v[34:35], off
	v_or_b32_e32 v34, 2, v30
	v_ashrrev_i32_e32 v35, 31, v34
	v_lshlrev_b64 v[34:35], 7, v[34:35]
	v_lshl_add_u64 v[34:35], v[28:29], 0, v[34:35]
	global_load_dword v42, v[34:35], off
	v_or_b32_e32 v34, 3, v30
	v_ashrrev_i32_e32 v35, 31, v34
	v_lshlrev_b64 v[34:35], 7, v[34:35]
	v_lshl_add_u64 v[34:35], v[28:29], 0, v[34:35]
	global_load_dword v45, v[34:35], off
	v_or_b32_e32 v34, 4, v30
	v_ashrrev_i32_e32 v35, 31, v34
	v_lshlrev_b64 v[34:35], 7, v[34:35]
	v_lshl_add_u64 v[34:35], v[28:29], 0, v[34:35]
	global_load_dword v47, v[34:35], off
	v_or_b32_e32 v34, 5, v30
	v_ashrrev_i32_e32 v35, 31, v34
	v_lshlrev_b64 v[34:35], 7, v[34:35]
	v_lshl_add_u64 v[34:35], v[28:29], 0, v[34:35]
	global_load_dword v49, v[34:35], off
	v_or_b32_e32 v34, 6, v30
	v_ashrrev_i32_e32 v35, 31, v34
	v_lshlrev_b64 v[34:35], 7, v[34:35]
	v_lshl_add_u64 v[34:35], v[28:29], 0, v[34:35]
	global_load_dword v51, v[34:35], off
	v_or_b32_e32 v34, 7, v30
	v_ashrrev_i32_e32 v35, 31, v34
	v_lshlrev_b64 v[34:35], 7, v[34:35]
	v_lshl_add_u64 v[34:35], v[28:29], 0, v[34:35]
	global_load_dword v34, v[34:35], off
	s_ashr_i32 s79, s78, 31
	s_lshl_b32 s88, s2, 6
	s_lshl_b64 s[8:9], s[78:79], 1
	s_add_u32 s8, s80, s8
	s_addc_u32 s9, s81, s9
	v_mov_b32_e32 v109, v3
	v_or_b32_e32 v110, s88, v114
	v_lshl_add_u64 v[16:17], s[8:9], 0, v[108:109]
	s_mov_b64 s[8:9], 0xc9000000
	v_ashrrev_i32_e32 v111, 31, v110
	v_lshl_add_u64 v[16:17], v[16:17], 0, s[8:9]
	s_and_b32 s8, s3, 0xffffffc0
	s_lshl_b32 s2, s8, 2
	s_add_i32 s2, s2, 0
	s_add_i32 s2, s2, 0x10800
	v_cmp_gt_u32_e32 vcc, 32, v112
	v_add_u32_e32 v2, s2, v2
	v_readlane_b32 s13, v254, 16
	s_waitcnt vmcnt(7)
	v_mul_f32_e32 v31, v1, v24
	s_waitcnt vmcnt(6)
	v_mul_f32_e32 v40, v41, v25
	v_cvt_pk_bf16_f32 v40, v31, v40
	s_waitcnt vmcnt(5)
	v_mul_f32_e32 v43, v42, v26
	v_lshlrev_b32_e32 v31, 16, v40
	v_fma_f32 v1, v1, v24, -v31
	v_and_b32_e32 v24, 0xffff0000, v40
	v_fma_f32 v24, v41, v25, -v24
	s_waitcnt vmcnt(4)
	v_mul_f32_e32 v46, v45, v27
	v_cvt_pk_bf16_f32 v44, v1, v24
	v_cvt_pk_bf16_f32 v41, v43, v46
	s_waitcnt vmcnt(3)
	v_mul_f32_e32 v48, v47, v20
	v_lshlrev_b32_e32 v1, 16, v41
	v_fma_f32 v1, v42, v26, -v1
	v_and_b32_e32 v24, 0xffff0000, v41
	v_fma_f32 v24, v45, v27, -v24
	s_waitcnt vmcnt(2)
	v_mul_f32_e32 v50, v49, v21
	v_cvt_pk_bf16_f32 v45, v1, v24
	v_cvt_pk_bf16_f32 v42, v48, v50
	s_waitcnt vmcnt(1)
	v_mul_f32_e32 v52, v51, v22
	v_lshlrev_b32_e32 v1, 16, v42
	v_fma_f32 v1, v47, v20, -v1
	v_and_b32_e32 v20, 0xffff0000, v42
	v_fma_f32 v20, v49, v21, -v20
	s_waitcnt vmcnt(0)
	v_mul_f32_e32 v35, v34, v23
	v_cvt_pk_bf16_f32 v46, v1, v20
	v_cvt_pk_bf16_f32 v43, v52, v35
	s_nop 0
	v_and_b32_e32 v20, 0xffff0000, v43
	v_lshlrev_b32_e32 v1, 16, v43
	v_fma_f32 v20, v34, v23, -v20
	v_fma_f32 v1, v51, v22, -v1
	v_cvt_pk_bf16_f32 v47, v1, v20
	v_or_b32_e32 v20, 16, v30
	v_or_b32_e32 v34, 17, v30
	v_ashrrev_i32_e32 v21, 31, v20
	v_ashrrev_i32_e32 v35, 31, v34
	v_lshlrev_b64 v[20:21], 7, v[20:21]
	v_lshlrev_b64 v[34:35], 7, v[34:35]
	v_lshl_add_u64 v[20:21], v[28:29], 0, v[20:21]
	v_lshl_add_u64 v[34:35], v[28:29], 0, v[34:35]
	global_load_dword v1, v[20:21], off
	s_nop 0
	global_load_dwordx4 v[20:23], v[32:33], off offset:80
	global_load_dwordx4 v[24:27], v[32:33], off offset:64
	global_load_dword v49, v[34:35], off
	v_or_b32_e32 v34, 18, v30
	v_ashrrev_i32_e32 v35, 31, v34
	v_lshlrev_b64 v[34:35], 7, v[34:35]
	v_lshl_add_u64 v[34:35], v[28:29], 0, v[34:35]
	global_load_dword v50, v[34:35], off
	v_or_b32_e32 v34, 19, v30
	v_ashrrev_i32_e32 v35, 31, v34
	v_lshlrev_b64 v[34:35], 7, v[34:35]
	v_lshl_add_u64 v[34:35], v[28:29], 0, v[34:35]
	global_load_dword v53, v[34:35], off
	v_or_b32_e32 v34, 20, v30
	v_ashrrev_i32_e32 v35, 31, v34
	v_lshlrev_b64 v[34:35], 7, v[34:35]
	v_lshl_add_u64 v[34:35], v[28:29], 0, v[34:35]
	global_load_dword v55, v[34:35], off
	v_or_b32_e32 v34, 21, v30
	v_ashrrev_i32_e32 v35, 31, v34
	v_lshlrev_b64 v[34:35], 7, v[34:35]
	v_lshl_add_u64 v[34:35], v[28:29], 0, v[34:35]
	global_load_dword v57, v[34:35], off
	v_or_b32_e32 v34, 22, v30
	v_ashrrev_i32_e32 v35, 31, v34
	v_lshlrev_b64 v[34:35], 7, v[34:35]
	v_lshl_add_u64 v[34:35], v[28:29], 0, v[34:35]
	global_load_dword v59, v[34:35], off
	v_or_b32_e32 v34, 23, v30
	v_ashrrev_i32_e32 v35, 31, v34
	v_lshlrev_b64 v[34:35], 7, v[34:35]
	v_lshl_add_u64 v[34:35], v[28:29], 0, v[34:35]
	global_load_dword v34, v[34:35], off
	s_waitcnt vmcnt(7)
	v_mul_f32_e32 v31, v1, v24
	s_waitcnt vmcnt(6)
	v_mul_f32_e32 v48, v49, v25
	v_cvt_pk_bf16_f32 v48, v31, v48
	s_waitcnt vmcnt(5)
	v_mul_f32_e32 v51, v50, v26
	v_lshlrev_b32_e32 v31, 16, v48
	v_fma_f32 v1, v1, v24, -v31
	v_and_b32_e32 v24, 0xffff0000, v48
	v_fma_f32 v24, v49, v25, -v24
	s_waitcnt vmcnt(4)
	v_mul_f32_e32 v54, v53, v27
	v_cvt_pk_bf16_f32 v52, v1, v24
	v_cvt_pk_bf16_f32 v49, v51, v54
	s_waitcnt vmcnt(3)
	v_mul_f32_e32 v56, v55, v20
	v_lshlrev_b32_e32 v1, 16, v49
	v_fma_f32 v1, v50, v26, -v1
	v_and_b32_e32 v24, 0xffff0000, v49
	v_fma_f32 v24, v53, v27, -v24
	s_waitcnt vmcnt(2)
	v_mul_f32_e32 v58, v57, v21
	v_cvt_pk_bf16_f32 v53, v1, v24
	v_cvt_pk_bf16_f32 v50, v56, v58
	s_waitcnt vmcnt(1)
	v_mul_f32_e32 v60, v59, v22
	v_lshlrev_b32_e32 v1, 16, v50
	v_fma_f32 v1, v55, v20, -v1
	v_and_b32_e32 v20, 0xffff0000, v50
	v_fma_f32 v20, v57, v21, -v20
	s_waitcnt vmcnt(0)
	v_mul_f32_e32 v35, v34, v23
	v_cvt_pk_bf16_f32 v54, v1, v20
	v_cvt_pk_bf16_f32 v51, v60, v35
	s_nop 0
	v_and_b32_e32 v20, 0xffff0000, v51
	v_lshlrev_b32_e32 v1, 16, v51
	v_fma_f32 v20, v34, v23, -v20
	v_fma_f32 v1, v59, v22, -v1
	v_cvt_pk_bf16_f32 v55, v1, v20
	v_or_b32_e32 v20, 32, v30
	v_or_b32_e32 v34, 33, v30
	v_ashrrev_i32_e32 v21, 31, v20
	v_ashrrev_i32_e32 v35, 31, v34
	v_lshlrev_b64 v[20:21], 7, v[20:21]
	v_lshlrev_b64 v[34:35], 7, v[34:35]
	v_lshl_add_u64 v[20:21], v[28:29], 0, v[20:21]
	v_lshl_add_u64 v[34:35], v[28:29], 0, v[34:35]
	global_load_dword v1, v[20:21], off
	s_nop 0
	global_load_dwordx4 v[20:23], v[32:33], off offset:144
	global_load_dwordx4 v[24:27], v[32:33], off offset:128
	global_load_dword v57, v[34:35], off
	v_or_b32_e32 v34, 34, v30
	v_ashrrev_i32_e32 v35, 31, v34
	v_lshlrev_b64 v[34:35], 7, v[34:35]
	v_lshl_add_u64 v[34:35], v[28:29], 0, v[34:35]
	global_load_dword v58, v[34:35], off
	v_or_b32_e32 v34, 35, v30
	v_ashrrev_i32_e32 v35, 31, v34
	v_lshlrev_b64 v[34:35], 7, v[34:35]
	v_lshl_add_u64 v[34:35], v[28:29], 0, v[34:35]
	global_load_dword v61, v[34:35], off
	v_or_b32_e32 v34, 36, v30
	v_ashrrev_i32_e32 v35, 31, v34
	v_lshlrev_b64 v[34:35], 7, v[34:35]
	v_lshl_add_u64 v[34:35], v[28:29], 0, v[34:35]
	global_load_dword v63, v[34:35], off
	v_or_b32_e32 v34, 37, v30
	v_ashrrev_i32_e32 v35, 31, v34
	v_lshlrev_b64 v[34:35], 7, v[34:35]
	v_lshl_add_u64 v[34:35], v[28:29], 0, v[34:35]
	global_load_dword v65, v[34:35], off
	v_or_b32_e32 v34, 38, v30
	v_ashrrev_i32_e32 v35, 31, v34
	v_lshlrev_b64 v[34:35], 7, v[34:35]
	v_lshl_add_u64 v[34:35], v[28:29], 0, v[34:35]
	global_load_dword v67, v[34:35], off
	v_or_b32_e32 v34, 39, v30
	v_ashrrev_i32_e32 v35, 31, v34
	v_lshlrev_b64 v[34:35], 7, v[34:35]
	v_lshl_add_u64 v[34:35], v[28:29], 0, v[34:35]
	global_load_dword v34, v[34:35], off
	s_waitcnt vmcnt(7)
	v_mul_f32_e32 v31, v1, v24
	s_waitcnt vmcnt(6)
	v_mul_f32_e32 v56, v57, v25
	v_cvt_pk_bf16_f32 v56, v31, v56
	s_waitcnt vmcnt(5)
	v_mul_f32_e32 v59, v58, v26
	v_lshlrev_b32_e32 v31, 16, v56
	v_fma_f32 v1, v1, v24, -v31
	v_and_b32_e32 v24, 0xffff0000, v56
	v_fma_f32 v24, v57, v25, -v24
	s_waitcnt vmcnt(4)
	v_mul_f32_e32 v62, v61, v27
	v_cvt_pk_bf16_f32 v60, v1, v24
	v_cvt_pk_bf16_f32 v57, v59, v62
	s_waitcnt vmcnt(3)
	v_mul_f32_e32 v64, v63, v20
	v_lshlrev_b32_e32 v1, 16, v57
	v_fma_f32 v1, v58, v26, -v1
	v_and_b32_e32 v24, 0xffff0000, v57
	v_fma_f32 v24, v61, v27, -v24
	s_waitcnt vmcnt(2)
	v_mul_f32_e32 v66, v65, v21
	v_cvt_pk_bf16_f32 v61, v1, v24
	v_cvt_pk_bf16_f32 v58, v64, v66
	s_waitcnt vmcnt(1)
	v_mul_f32_e32 v68, v67, v22
	v_lshlrev_b32_e32 v1, 16, v58
	v_fma_f32 v1, v63, v20, -v1
	v_and_b32_e32 v20, 0xffff0000, v58
	v_fma_f32 v20, v65, v21, -v20
	s_waitcnt vmcnt(0)
	v_mul_f32_e32 v35, v34, v23
	v_cvt_pk_bf16_f32 v62, v1, v20
	v_cvt_pk_bf16_f32 v59, v68, v35
	s_nop 0
	v_and_b32_e32 v20, 0xffff0000, v59
	v_lshlrev_b32_e32 v1, 16, v59
	v_fma_f32 v20, v34, v23, -v20
	v_fma_f32 v1, v67, v22, -v1
	v_cvt_pk_bf16_f32 v63, v1, v20
	v_or_b32_e32 v20, 48, v30
	v_or_b32_e32 v34, 49, v30
	v_ashrrev_i32_e32 v21, 31, v20
	v_ashrrev_i32_e32 v35, 31, v34
	v_lshlrev_b64 v[20:21], 7, v[20:21]
	v_lshlrev_b64 v[34:35], 7, v[34:35]
	v_lshl_add_u64 v[20:21], v[28:29], 0, v[20:21]
	v_lshl_add_u64 v[34:35], v[28:29], 0, v[34:35]
	global_load_dword v1, v[20:21], off
	s_nop 0
	global_load_dwordx4 v[20:23], v[32:33], off offset:208
	global_load_dwordx4 v[24:27], v[32:33], off offset:192
	global_load_dword v65, v[34:35], off
	v_or_b32_e32 v34, 50, v30
	v_ashrrev_i32_e32 v35, 31, v34
	v_lshlrev_b64 v[34:35], 7, v[34:35]
	v_lshl_add_u64 v[34:35], v[28:29], 0, v[34:35]
	global_load_dword v66, v[34:35], off
	v_or_b32_e32 v34, 51, v30
	v_ashrrev_i32_e32 v35, 31, v34
	v_lshlrev_b64 v[34:35], 7, v[34:35]
	v_lshl_add_u64 v[34:35], v[28:29], 0, v[34:35]
	global_load_dword v69, v[34:35], off
	v_or_b32_e32 v34, 52, v30
	v_ashrrev_i32_e32 v35, 31, v34
	v_lshlrev_b64 v[34:35], 7, v[34:35]
	v_lshl_add_u64 v[34:35], v[28:29], 0, v[34:35]
	global_load_dword v71, v[34:35], off
	v_or_b32_e32 v34, 53, v30
	v_ashrrev_i32_e32 v35, 31, v34
	v_lshlrev_b64 v[34:35], 7, v[34:35]
	v_lshl_add_u64 v[34:35], v[28:29], 0, v[34:35]
	global_load_dword v73, v[34:35], off
	v_or_b32_e32 v34, 54, v30
	v_ashrrev_i32_e32 v35, 31, v34
	v_lshlrev_b64 v[34:35], 7, v[34:35]
	v_lshl_add_u64 v[34:35], v[28:29], 0, v[34:35]
	global_load_dword v75, v[34:35], off
	v_or_b32_e32 v34, 55, v30
	v_ashrrev_i32_e32 v35, 31, v34
	v_lshlrev_b64 v[34:35], 7, v[34:35]
	v_lshl_add_u64 v[34:35], v[28:29], 0, v[34:35]
	global_load_dword v34, v[34:35], off
	s_waitcnt vmcnt(7)
	v_mul_f32_e32 v31, v1, v24
	s_waitcnt vmcnt(6)
	v_mul_f32_e32 v64, v65, v25
	v_cvt_pk_bf16_f32 v64, v31, v64
	s_waitcnt vmcnt(5)
	v_mul_f32_e32 v67, v66, v26
	v_lshlrev_b32_e32 v31, 16, v64
	v_fma_f32 v1, v1, v24, -v31
	v_and_b32_e32 v24, 0xffff0000, v64
	v_fma_f32 v24, v65, v25, -v24
	s_waitcnt vmcnt(4)
	v_mul_f32_e32 v70, v69, v27
	v_cvt_pk_bf16_f32 v68, v1, v24
	v_cvt_pk_bf16_f32 v65, v67, v70
	s_waitcnt vmcnt(3)
	v_mul_f32_e32 v72, v71, v20
	v_lshlrev_b32_e32 v1, 16, v65
	v_fma_f32 v1, v66, v26, -v1
	v_and_b32_e32 v24, 0xffff0000, v65
	v_fma_f32 v24, v69, v27, -v24
	s_waitcnt vmcnt(2)
	v_mul_f32_e32 v74, v73, v21
	v_cvt_pk_bf16_f32 v69, v1, v24
	v_cvt_pk_bf16_f32 v66, v72, v74
	s_waitcnt vmcnt(1)
	v_mul_f32_e32 v76, v75, v22
	v_lshlrev_b32_e32 v1, 16, v66
	v_fma_f32 v1, v71, v20, -v1
	v_and_b32_e32 v20, 0xffff0000, v66
	v_fma_f32 v20, v73, v21, -v20
	s_waitcnt vmcnt(0)
	v_mul_f32_e32 v35, v34, v23
	v_cvt_pk_bf16_f32 v70, v1, v20
	v_cvt_pk_bf16_f32 v67, v76, v35
	s_nop 0
	v_and_b32_e32 v20, 0xffff0000, v67
	v_lshlrev_b32_e32 v1, 16, v67
	v_fma_f32 v20, v34, v23, -v20
	v_fma_f32 v1, v75, v22, -v1
	v_cvt_pk_bf16_f32 v71, v1, v20
	v_or_b32_e32 v20, 64, v30
	v_or_b32_e32 v34, 0x41, v30
	v_ashrrev_i32_e32 v21, 31, v20
	v_ashrrev_i32_e32 v35, 31, v34
	v_lshlrev_b64 v[20:21], 7, v[20:21]
	v_lshlrev_b64 v[34:35], 7, v[34:35]
	v_lshl_add_u64 v[20:21], v[28:29], 0, v[20:21]
	v_lshl_add_u64 v[34:35], v[28:29], 0, v[34:35]
	global_load_dword v1, v[20:21], off
	s_nop 0
	global_load_dwordx4 v[20:23], v[32:33], off offset:272
	global_load_dwordx4 v[24:27], v[32:33], off offset:256
	global_load_dword v73, v[34:35], off
	v_or_b32_e32 v34, 0x42, v30
	v_ashrrev_i32_e32 v35, 31, v34
	v_lshlrev_b64 v[34:35], 7, v[34:35]
	v_lshl_add_u64 v[34:35], v[28:29], 0, v[34:35]
	global_load_dword v74, v[34:35], off
	v_or_b32_e32 v34, 0x43, v30
	v_ashrrev_i32_e32 v35, 31, v34
	v_lshlrev_b64 v[34:35], 7, v[34:35]
	v_lshl_add_u64 v[34:35], v[28:29], 0, v[34:35]
	global_load_dword v77, v[34:35], off
	v_or_b32_e32 v34, 0x44, v30
	v_ashrrev_i32_e32 v35, 31, v34
	v_lshlrev_b64 v[34:35], 7, v[34:35]
	v_lshl_add_u64 v[34:35], v[28:29], 0, v[34:35]
	global_load_dword v79, v[34:35], off
	v_or_b32_e32 v34, 0x45, v30
	v_ashrrev_i32_e32 v35, 31, v34
	v_lshlrev_b64 v[34:35], 7, v[34:35]
	v_lshl_add_u64 v[34:35], v[28:29], 0, v[34:35]
	global_load_dword v81, v[34:35], off
	v_or_b32_e32 v34, 0x46, v30
	v_ashrrev_i32_e32 v35, 31, v34
	v_lshlrev_b64 v[34:35], 7, v[34:35]
	v_lshl_add_u64 v[34:35], v[28:29], 0, v[34:35]
	global_load_dword v83, v[34:35], off
	v_or_b32_e32 v34, 0x47, v30
	v_ashrrev_i32_e32 v35, 31, v34
	v_lshlrev_b64 v[34:35], 7, v[34:35]
	v_lshl_add_u64 v[34:35], v[28:29], 0, v[34:35]
	global_load_dword v34, v[34:35], off
	s_waitcnt vmcnt(7)
	v_mul_f32_e32 v31, v1, v24
	s_waitcnt vmcnt(6)
	v_mul_f32_e32 v72, v73, v25
	v_cvt_pk_bf16_f32 v72, v31, v72
	s_waitcnt vmcnt(5)
	v_mul_f32_e32 v75, v74, v26
	v_lshlrev_b32_e32 v31, 16, v72
	v_fma_f32 v1, v1, v24, -v31
	v_and_b32_e32 v24, 0xffff0000, v72
	v_fma_f32 v24, v73, v25, -v24
	s_waitcnt vmcnt(4)
	v_mul_f32_e32 v78, v77, v27
	v_cvt_pk_bf16_f32 v76, v1, v24
	v_cvt_pk_bf16_f32 v73, v75, v78
	s_waitcnt vmcnt(3)
	v_mul_f32_e32 v80, v79, v20
	v_lshlrev_b32_e32 v1, 16, v73
	v_fma_f32 v1, v74, v26, -v1
	v_and_b32_e32 v24, 0xffff0000, v73
	v_fma_f32 v24, v77, v27, -v24
	s_waitcnt vmcnt(2)
	v_mul_f32_e32 v82, v81, v21
	v_cvt_pk_bf16_f32 v77, v1, v24
	v_cvt_pk_bf16_f32 v74, v80, v82
	s_waitcnt vmcnt(1)
	v_mul_f32_e32 v84, v83, v22
	v_lshlrev_b32_e32 v1, 16, v74
	v_fma_f32 v1, v79, v20, -v1
	v_and_b32_e32 v20, 0xffff0000, v74
	v_fma_f32 v20, v81, v21, -v20
	s_waitcnt vmcnt(0)
	v_mul_f32_e32 v35, v34, v23
	v_cvt_pk_bf16_f32 v78, v1, v20
	v_cvt_pk_bf16_f32 v75, v84, v35
	s_nop 0
	v_and_b32_e32 v20, 0xffff0000, v75
	v_lshlrev_b32_e32 v1, 16, v75
	v_fma_f32 v20, v34, v23, -v20
	v_fma_f32 v1, v83, v22, -v1
	v_cvt_pk_bf16_f32 v79, v1, v20
	v_or_b32_e32 v20, 0x50, v30
	v_or_b32_e32 v34, 0x51, v30
	v_ashrrev_i32_e32 v21, 31, v20
	v_ashrrev_i32_e32 v35, 31, v34
	v_lshlrev_b64 v[20:21], 7, v[20:21]
	v_lshlrev_b64 v[34:35], 7, v[34:35]
	v_lshl_add_u64 v[20:21], v[28:29], 0, v[20:21]
	v_lshl_add_u64 v[34:35], v[28:29], 0, v[34:35]
	global_load_dword v1, v[20:21], off
	s_nop 0
	global_load_dwordx4 v[20:23], v[32:33], off offset:336
	global_load_dwordx4 v[24:27], v[32:33], off offset:320
	global_load_dword v81, v[34:35], off
	v_or_b32_e32 v34, 0x52, v30
	v_ashrrev_i32_e32 v35, 31, v34
	v_lshlrev_b64 v[34:35], 7, v[34:35]
	v_lshl_add_u64 v[34:35], v[28:29], 0, v[34:35]
	global_load_dword v82, v[34:35], off
	v_or_b32_e32 v34, 0x53, v30
	v_ashrrev_i32_e32 v35, 31, v34
	v_lshlrev_b64 v[34:35], 7, v[34:35]
	v_lshl_add_u64 v[34:35], v[28:29], 0, v[34:35]
	global_load_dword v85, v[34:35], off
	v_or_b32_e32 v34, 0x54, v30
	v_ashrrev_i32_e32 v35, 31, v34
	v_lshlrev_b64 v[34:35], 7, v[34:35]
	v_lshl_add_u64 v[34:35], v[28:29], 0, v[34:35]
	global_load_dword v87, v[34:35], off
	v_or_b32_e32 v34, 0x55, v30
	v_ashrrev_i32_e32 v35, 31, v34
	v_lshlrev_b64 v[34:35], 7, v[34:35]
	v_lshl_add_u64 v[34:35], v[28:29], 0, v[34:35]
	global_load_dword v89, v[34:35], off
	v_or_b32_e32 v34, 0x56, v30
	v_ashrrev_i32_e32 v35, 31, v34
	v_lshlrev_b64 v[34:35], 7, v[34:35]
	v_lshl_add_u64 v[34:35], v[28:29], 0, v[34:35]
	global_load_dword v91, v[34:35], off
	v_or_b32_e32 v34, 0x57, v30
	v_ashrrev_i32_e32 v35, 31, v34
	v_lshlrev_b64 v[34:35], 7, v[34:35]
	v_lshl_add_u64 v[34:35], v[28:29], 0, v[34:35]
	global_load_dword v34, v[34:35], off
	s_waitcnt vmcnt(7)
	v_mul_f32_e32 v31, v1, v24
	s_waitcnt vmcnt(6)
	v_mul_f32_e32 v80, v81, v25
	v_cvt_pk_bf16_f32 v80, v31, v80
	s_waitcnt vmcnt(5)
	v_mul_f32_e32 v83, v82, v26
	v_lshlrev_b32_e32 v31, 16, v80
	v_fma_f32 v1, v1, v24, -v31
	v_and_b32_e32 v24, 0xffff0000, v80
	v_fma_f32 v24, v81, v25, -v24
	s_waitcnt vmcnt(4)
	v_mul_f32_e32 v86, v85, v27
	v_cvt_pk_bf16_f32 v84, v1, v24
	v_cvt_pk_bf16_f32 v81, v83, v86
	s_waitcnt vmcnt(3)
	v_mul_f32_e32 v88, v87, v20
	v_lshlrev_b32_e32 v1, 16, v81
	v_fma_f32 v1, v82, v26, -v1
	v_and_b32_e32 v24, 0xffff0000, v81
	v_fma_f32 v24, v85, v27, -v24
	s_waitcnt vmcnt(2)
	v_mul_f32_e32 v90, v89, v21
	v_cvt_pk_bf16_f32 v85, v1, v24
	v_cvt_pk_bf16_f32 v82, v88, v90
	s_waitcnt vmcnt(1)
	v_mul_f32_e32 v92, v91, v22
	v_lshlrev_b32_e32 v1, 16, v82
	v_fma_f32 v1, v87, v20, -v1
	v_and_b32_e32 v20, 0xffff0000, v82
	v_fma_f32 v20, v89, v21, -v20
	s_waitcnt vmcnt(0)
	v_mul_f32_e32 v35, v34, v23
	v_cvt_pk_bf16_f32 v86, v1, v20
	v_cvt_pk_bf16_f32 v83, v92, v35
	s_nop 0
	v_and_b32_e32 v20, 0xffff0000, v83
	v_lshlrev_b32_e32 v1, 16, v83
	v_fma_f32 v20, v34, v23, -v20
	v_fma_f32 v1, v91, v22, -v1
	v_cvt_pk_bf16_f32 v87, v1, v20
	v_or_b32_e32 v20, 0x60, v30
	v_or_b32_e32 v34, 0x61, v30
	v_ashrrev_i32_e32 v21, 31, v20
	v_ashrrev_i32_e32 v35, 31, v34
	v_lshlrev_b64 v[20:21], 7, v[20:21]
	v_lshlrev_b64 v[34:35], 7, v[34:35]
	v_lshl_add_u64 v[20:21], v[28:29], 0, v[20:21]
	v_lshl_add_u64 v[34:35], v[28:29], 0, v[34:35]
	global_load_dword v1, v[20:21], off
	s_nop 0
	global_load_dwordx4 v[20:23], v[32:33], off offset:400
	global_load_dwordx4 v[24:27], v[32:33], off offset:384
	global_load_dword v88, v[34:35], off
	v_or_b32_e32 v34, 0x62, v30
	v_ashrrev_i32_e32 v35, 31, v34
	v_lshlrev_b64 v[34:35], 7, v[34:35]
	v_lshl_add_u64 v[34:35], v[28:29], 0, v[34:35]
	global_load_dword v90, v[34:35], off
	v_or_b32_e32 v34, 0x63, v30
	v_ashrrev_i32_e32 v35, 31, v34
	v_lshlrev_b64 v[34:35], 7, v[34:35]
	v_lshl_add_u64 v[34:35], v[28:29], 0, v[34:35]
	global_load_dword v92, v[34:35], off
	v_or_b32_e32 v34, 0x64, v30
	v_ashrrev_i32_e32 v35, 31, v34
	v_lshlrev_b64 v[34:35], 7, v[34:35]
	v_lshl_add_u64 v[34:35], v[28:29], 0, v[34:35]
	global_load_dword v94, v[34:35], off
	v_or_b32_e32 v34, 0x65, v30
	v_ashrrev_i32_e32 v35, 31, v34
	v_lshlrev_b64 v[34:35], 7, v[34:35]
	v_lshl_add_u64 v[34:35], v[28:29], 0, v[34:35]
	global_load_dword v99, v[34:35], off
	v_or_b32_e32 v34, 0x66, v30
	v_ashrrev_i32_e32 v35, 31, v34
	v_lshlrev_b64 v[34:35], 7, v[34:35]
	v_lshl_add_u64 v[34:35], v[28:29], 0, v[34:35]
	global_load_dword v103, v[34:35], off
	v_or_b32_e32 v34, 0x67, v30
	v_ashrrev_i32_e32 v35, 31, v34
	v_lshlrev_b64 v[34:35], 7, v[34:35]
	v_lshl_add_u64 v[34:35], v[28:29], 0, v[34:35]
	global_load_dword v34, v[34:35], off
	s_waitcnt vmcnt(7)
	v_mul_f32_e32 v31, v1, v24
	s_waitcnt vmcnt(6)
	v_mul_f32_e32 v89, v88, v25
	v_cvt_pk_bf16_f32 v96, v31, v89
	s_waitcnt vmcnt(5)
	v_mul_f32_e32 v91, v90, v26
	v_lshlrev_b32_e32 v31, 16, v96
	v_fma_f32 v1, v1, v24, -v31
	v_and_b32_e32 v24, 0xffff0000, v96
	v_fma_f32 v24, v88, v25, -v24
	s_waitcnt vmcnt(4)
	v_mul_f32_e32 v93, v92, v27
	v_cvt_pk_bf16_f32 v100, v1, v24
	v_cvt_pk_bf16_f32 v97, v91, v93
	s_waitcnt vmcnt(3)
	v_mul_f32_e32 v95, v94, v20
	v_lshlrev_b32_e32 v1, 16, v97
	v_fma_f32 v1, v90, v26, -v1
	v_and_b32_e32 v24, 0xffff0000, v97
	v_fma_f32 v24, v92, v27, -v24
	s_waitcnt vmcnt(2)
	v_mul_f32_e32 v98, v99, v21
	v_cvt_pk_bf16_f32 v101, v1, v24
	v_cvt_pk_bf16_f32 v98, v95, v98
	s_waitcnt vmcnt(1)
	v_mul_f32_e32 v104, v103, v22
	v_lshlrev_b32_e32 v1, 16, v98
	v_fma_f32 v1, v94, v20, -v1
	v_and_b32_e32 v20, 0xffff0000, v98
	v_fma_f32 v20, v99, v21, -v20
	s_waitcnt vmcnt(0)
	v_mul_f32_e32 v35, v34, v23
	v_cvt_pk_bf16_f32 v102, v1, v20
	v_cvt_pk_bf16_f32 v99, v104, v35
	s_nop 0
	v_and_b32_e32 v20, 0xffff0000, v99
	v_lshlrev_b32_e32 v1, 16, v99
	v_fma_f32 v20, v34, v23, -v20
	v_fma_f32 v1, v103, v22, -v1
	v_cvt_pk_bf16_f32 v103, v1, v20
	v_or_b32_e32 v20, 0x70, v30
	v_ashrrev_i32_e32 v21, 31, v20
	v_lshlrev_b64 v[20:21], 7, v[20:21]
	v_lshl_add_u64 v[20:21], v[28:29], 0, v[20:21]
	global_load_dword v1, v[20:21], off
	s_nop 0
	global_load_dwordx4 v[20:23], v[32:33], off offset:464
	global_load_dwordx4 v[24:27], v[32:33], off offset:448
	v_or_b32_e32 v32, 0x71, v30
	v_ashrrev_i32_e32 v33, 31, v32
	v_lshlrev_b64 v[32:33], 7, v[32:33]
	v_lshl_add_u64 v[32:33], v[28:29], 0, v[32:33]
	global_load_dword v35, v[32:33], off
	v_or_b32_e32 v32, 0x72, v30
	v_ashrrev_i32_e32 v33, 31, v32
	v_lshlrev_b64 v[32:33], 7, v[32:33]
	v_lshl_add_u64 v[32:33], v[28:29], 0, v[32:33]
	global_load_dword v89, v[32:33], off
	v_or_b32_e32 v32, 0x73, v30
	v_ashrrev_i32_e32 v33, 31, v32
	v_lshlrev_b64 v[32:33], 7, v[32:33]
	v_lshl_add_u64 v[32:33], v[28:29], 0, v[32:33]
	global_load_dword v91, v[32:33], off
	v_or_b32_e32 v32, 0x74, v30
	v_ashrrev_i32_e32 v33, 31, v32
	v_lshlrev_b64 v[32:33], 7, v[32:33]
	v_lshl_add_u64 v[32:33], v[28:29], 0, v[32:33]
	global_load_dword v95, v[32:33], off
	v_or_b32_e32 v32, 0x75, v30
	v_ashrrev_i32_e32 v33, 31, v32
	v_lshlrev_b64 v[32:33], 7, v[32:33]
	v_lshl_add_u64 v[32:33], v[28:29], 0, v[32:33]
	global_load_dword v104, v[32:33], off
	v_or_b32_e32 v32, 0x76, v30
	v_or_b32_e32 v30, 0x77, v30
	v_ashrrev_i32_e32 v33, 31, v32
	v_ashrrev_i32_e32 v31, 31, v30
	v_lshlrev_b64 v[32:33], 7, v[32:33]
	v_lshlrev_b64 v[30:31], 7, v[30:31]
	v_lshl_add_u64 v[32:33], v[28:29], 0, v[32:33]
	v_lshl_add_u64 v[28:29], v[28:29], 0, v[30:31]
	global_load_dword v32, v[32:33], off
	s_waitcnt vmcnt(6)
	v_mul_f32_e32 v34, v1, v24
	global_load_dword v28, v[28:29], off
	s_waitcnt vmcnt(6)
	v_mul_f32_e32 v88, v35, v25
	v_cvt_pk_bf16_f32 v92, v34, v88
	s_waitcnt vmcnt(5)
	v_mul_f32_e32 v90, v89, v26
	v_lshlrev_b32_e32 v30, 16, v92
	v_fma_f32 v1, v1, v24, -v30
	v_and_b32_e32 v24, 0xffff0000, v92
	v_fma_f32 v24, v35, v25, -v24
	s_waitcnt vmcnt(4)
	v_mul_f32_e32 v93, v91, v27
	v_cvt_pk_bf16_f32 v88, v1, v24
	v_cvt_pk_bf16_f32 v93, v90, v93
	s_waitcnt vmcnt(3)
	v_mul_f32_e32 v94, v95, v20
	v_lshlrev_b32_e32 v1, 16, v93
	v_fma_f32 v1, v89, v26, -v1
	v_and_b32_e32 v24, 0xffff0000, v93
	v_fma_f32 v24, v91, v27, -v24
	s_waitcnt vmcnt(2)
	v_mul_f32_e32 v105, v104, v21
	v_cvt_pk_bf16_f32 v89, v1, v24
	v_cvt_pk_bf16_f32 v94, v94, v105
	s_waitcnt vmcnt(1)
	v_mul_f32_e32 v33, v32, v22
	v_lshlrev_b32_e32 v1, 16, v94
	v_fma_f32 v1, v95, v20, -v1
	v_and_b32_e32 v20, 0xffff0000, v94
	v_fma_f32 v20, v104, v21, -v20
	v_cvt_pk_bf16_f32 v90, v1, v20
	s_waitcnt vmcnt(0)
	v_mul_f32_e32 v29, v28, v23
	v_cvt_pk_bf16_f32 v95, v33, v29
	s_nop 0
	v_and_b32_e32 v20, 0xffff0000, v95
	v_lshlrev_b32_e32 v1, 16, v95
	v_fma_f32 v20, v28, v23, -v20
	v_fma_f32 v1, v32, v22, -v1
	v_cvt_pk_bf16_f32 v91, v1, v20
	v_lshlrev_b64 v[20:21], 11, v[110:111]
	v_lshl_add_u64 v[104:105], v[16:17], 0, v[20:21]
	global_load_dwordx4 v[120:123], v[104:105], off
	global_load_dwordx4 v[124:127], v[104:105], off offset:32
	global_load_dwordx4 v[128:131], v[104:105], off offset:64
	global_load_dwordx4 v[132:135], v[104:105], off offset:96
	global_load_dwordx4 v[136:139], v[104:105], off offset:128
	global_load_dwordx4 v[140:143], v[104:105], off offset:160
	global_load_dwordx4 v[144:147], v[104:105], off offset:192
	global_load_dwordx4 v[148:151], v[104:105], off offset:224
	s_mov_b32 s100, 0x10000
	s_mov_b32 s101, 0
	v_lshl_add_u64 v[184:185], v[104:105], 0, s[100:101]
	global_load_dwordx4 v[152:155], v[184:185], off
	global_load_dwordx4 v[156:159], v[184:185], off offset:32
	global_load_dwordx4 v[160:163], v[184:185], off offset:64
	global_load_dwordx4 v[164:167], v[184:185], off offset:96
	global_load_dwordx4 v[168:171], v[184:185], off offset:128
	global_load_dwordx4 v[172:175], v[184:185], off offset:160
	global_load_dwordx4 v[176:179], v[184:185], off offset:192
	global_load_dwordx4 v[180:183], v[184:185], off offset:224
	s_waitcnt vmcnt(15)
	v_mov_b32_e32 v116, v120
	v_mov_b32_e32 v117, v121
	v_mov_b32_e32 v118, v122
	v_mov_b32_e32 v119, v123
	v_and_b32_e32 v20, 0xffff0000, v116
	v_lshlrev_b32_e32 v1, 16, v116
	v_mul_f32_e32 v20, v20, v20
	v_and_b32_e32 v21, 0xffff0000, v117
	v_fmac_f32_e32 v20, v1, v1
	v_lshlrev_b32_e32 v1, 16, v117
	v_mul_f32_e32 v21, v21, v21
	v_fmac_f32_e32 v21, v1, v1
	v_add_f32_e32 v1, v20, v21
	v_and_b32_e32 v21, 0xffff0000, v118
	v_lshlrev_b32_e32 v20, 16, v118
	v_mul_f32_e32 v21, v21, v21
	v_fmac_f32_e32 v21, v20, v20
	v_add_f32_e32 v1, v21, v1
	v_and_b32_e32 v21, 0xffff0000, v119
	v_lshlrev_b32_e32 v20, 16, v119
	v_mul_f32_e32 v21, v21, v21
	v_fmac_f32_e32 v21, v20, v20
	v_add_f32_e32 v1, v21, v1
	v_mfma_f32_32x32x16_bf16 v[20:35], v[40:43], v[116:119], 0
	v_mfma_f32_32x32x16_bf16 v[20:35], v[44:47], v[116:119], v[20:35]
	s_waitcnt vmcnt(14)
	v_mov_b32_e32 v116, v124
	v_mov_b32_e32 v117, v125
	v_mov_b32_e32 v118, v126
	v_mov_b32_e32 v119, v127
	v_and_b32_e32 v107, 0xffff0000, v116
	v_lshlrev_b32_e32 v106, 16, v116
	v_mul_f32_e32 v107, v107, v107
	v_mfma_f32_32x32x16_bf16 v[20:35], v[48:51], v[116:119], v[20:35]
	v_fmac_f32_e32 v107, v106, v106
	v_add_f32_e32 v1, v1, v107
	v_and_b32_e32 v107, 0xffff0000, v117
	v_lshlrev_b32_e32 v106, 16, v117
	v_mul_f32_e32 v107, v107, v107
	v_fmac_f32_e32 v107, v106, v106
	v_add_f32_e32 v1, v107, v1
	v_and_b32_e32 v107, 0xffff0000, v118
	v_lshlrev_b32_e32 v106, 16, v118
	v_mul_f32_e32 v107, v107, v107
	v_fmac_f32_e32 v107, v106, v106
	v_add_f32_e32 v1, v107, v1
	v_lshlrev_b32_e32 v106, 16, v119
	v_and_b32_e32 v107, 0xffff0000, v119
	v_mfma_f32_32x32x16_bf16 v[20:35], v[52:55], v[116:119], v[20:35]
	v_mul_f32_e32 v107, v107, v107
	v_fmac_f32_e32 v107, v106, v106
	v_add_f32_e32 v1, v107, v1
	s_waitcnt vmcnt(13)
	v_mov_b32_e32 v116, v128
	v_mov_b32_e32 v117, v129
	v_mov_b32_e32 v118, v130
	v_mov_b32_e32 v119, v131
	v_and_b32_e32 v107, 0xffff0000, v116
	v_lshlrev_b32_e32 v106, 16, v116
	v_mul_f32_e32 v107, v107, v107
	v_mfma_f32_32x32x16_bf16 v[20:35], v[56:59], v[116:119], v[20:35]
	v_fmac_f32_e32 v107, v106, v106
	v_add_f32_e32 v1, v107, v1
	v_and_b32_e32 v107, 0xffff0000, v117
	v_lshlrev_b32_e32 v106, 16, v117
	v_mul_f32_e32 v107, v107, v107
	v_fmac_f32_e32 v107, v106, v106
	v_add_f32_e32 v1, v107, v1
	v_and_b32_e32 v107, 0xffff0000, v118
	v_lshlrev_b32_e32 v106, 16, v118
	v_mul_f32_e32 v107, v107, v107
	v_fmac_f32_e32 v107, v106, v106
	v_add_f32_e32 v1, v107, v1
	v_lshlrev_b32_e32 v106, 16, v119
	v_and_b32_e32 v107, 0xffff0000, v119
	v_mfma_f32_32x32x16_bf16 v[20:35], v[60:63], v[116:119], v[20:35]
	v_mul_f32_e32 v107, v107, v107
	v_fmac_f32_e32 v107, v106, v106
	v_add_f32_e32 v1, v107, v1
	s_waitcnt vmcnt(12)
	v_mov_b32_e32 v116, v132
	v_mov_b32_e32 v117, v133
	v_mov_b32_e32 v118, v134
	v_mov_b32_e32 v119, v135
	v_and_b32_e32 v107, 0xffff0000, v116
	v_lshlrev_b32_e32 v106, 16, v116
	v_mul_f32_e32 v107, v107, v107
	v_mfma_f32_32x32x16_bf16 v[20:35], v[64:67], v[116:119], v[20:35]
	v_fmac_f32_e32 v107, v106, v106
	v_add_f32_e32 v1, v107, v1
	v_and_b32_e32 v107, 0xffff0000, v117
	v_lshlrev_b32_e32 v106, 16, v117
	v_mul_f32_e32 v107, v107, v107
	v_fmac_f32_e32 v107, v106, v106
	v_add_f32_e32 v1, v107, v1
	v_and_b32_e32 v107, 0xffff0000, v118
	v_lshlrev_b32_e32 v106, 16, v118
	v_mul_f32_e32 v107, v107, v107
	v_fmac_f32_e32 v107, v106, v106
	v_add_f32_e32 v1, v107, v1
	v_lshlrev_b32_e32 v106, 16, v119
	v_and_b32_e32 v107, 0xffff0000, v119
	v_mfma_f32_32x32x16_bf16 v[20:35], v[68:71], v[116:119], v[20:35]
	v_mul_f32_e32 v107, v107, v107
	v_fmac_f32_e32 v107, v106, v106
	v_add_f32_e32 v1, v107, v1
	s_waitcnt vmcnt(11)
	v_mov_b32_e32 v116, v136
	v_mov_b32_e32 v117, v137
	v_mov_b32_e32 v118, v138
	v_mov_b32_e32 v119, v139
	v_and_b32_e32 v107, 0xffff0000, v116
	v_lshlrev_b32_e32 v106, 16, v116
	v_mul_f32_e32 v107, v107, v107
	v_mfma_f32_32x32x16_bf16 v[20:35], v[72:75], v[116:119], v[20:35]
	v_fmac_f32_e32 v107, v106, v106
	v_add_f32_e32 v1, v107, v1
	v_and_b32_e32 v107, 0xffff0000, v117
	v_lshlrev_b32_e32 v106, 16, v117
	v_mul_f32_e32 v107, v107, v107
	v_fmac_f32_e32 v107, v106, v106
	v_add_f32_e32 v1, v107, v1
	v_and_b32_e32 v107, 0xffff0000, v118
	v_lshlrev_b32_e32 v106, 16, v118
	v_mul_f32_e32 v107, v107, v107
	v_fmac_f32_e32 v107, v106, v106
	v_add_f32_e32 v1, v107, v1
	v_lshlrev_b32_e32 v106, 16, v119
	v_and_b32_e32 v107, 0xffff0000, v119
	v_mfma_f32_32x32x16_bf16 v[20:35], v[76:79], v[116:119], v[20:35]
	v_mul_f32_e32 v107, v107, v107
	v_fmac_f32_e32 v107, v106, v106
	v_add_f32_e32 v1, v107, v1
	s_waitcnt vmcnt(10)
	v_mov_b32_e32 v116, v140
	v_mov_b32_e32 v117, v141
	v_mov_b32_e32 v118, v142
	v_mov_b32_e32 v119, v143
	v_and_b32_e32 v107, 0xffff0000, v116
	v_lshlrev_b32_e32 v106, 16, v116
	v_mul_f32_e32 v107, v107, v107
	v_mfma_f32_32x32x16_bf16 v[20:35], v[80:83], v[116:119], v[20:35]
	v_fmac_f32_e32 v107, v106, v106
	v_add_f32_e32 v1, v107, v1
	v_and_b32_e32 v107, 0xffff0000, v117
	v_lshlrev_b32_e32 v106, 16, v117
	v_mul_f32_e32 v107, v107, v107
	v_fmac_f32_e32 v107, v106, v106
	v_add_f32_e32 v1, v107, v1
	v_and_b32_e32 v107, 0xffff0000, v118
	v_lshlrev_b32_e32 v106, 16, v118
	v_mul_f32_e32 v107, v107, v107
	v_fmac_f32_e32 v107, v106, v106
	v_add_f32_e32 v1, v107, v1
	v_lshlrev_b32_e32 v106, 16, v119
	v_and_b32_e32 v107, 0xffff0000, v119
	v_mfma_f32_32x32x16_bf16 v[20:35], v[84:87], v[116:119], v[20:35]
	v_mul_f32_e32 v107, v107, v107
	v_fmac_f32_e32 v107, v106, v106
	v_add_f32_e32 v1, v107, v1
	s_waitcnt vmcnt(9)
	v_mov_b32_e32 v116, v144
	v_mov_b32_e32 v117, v145
	v_mov_b32_e32 v118, v146
	v_mov_b32_e32 v119, v147
	v_and_b32_e32 v107, 0xffff0000, v116
	v_lshlrev_b32_e32 v106, 16, v116
	v_mul_f32_e32 v107, v107, v107
	v_fmac_f32_e32 v107, v106, v106
	v_add_f32_e32 v1, v107, v1
	v_and_b32_e32 v107, 0xffff0000, v117
	v_lshlrev_b32_e32 v106, 16, v117
	v_mul_f32_e32 v107, v107, v107
	v_fmac_f32_e32 v107, v106, v106
	v_add_f32_e32 v1, v107, v1
	v_and_b32_e32 v107, 0xffff0000, v118
	v_lshlrev_b32_e32 v106, 16, v118
	v_mul_f32_e32 v107, v107, v107
	v_fmac_f32_e32 v107, v106, v106
	v_add_f32_e32 v1, v107, v1
	v_and_b32_e32 v107, 0xffff0000, v119
	v_lshlrev_b32_e32 v106, 16, v119
	v_mul_f32_e32 v107, v107, v107
	v_fmac_f32_e32 v107, v106, v106
	v_add_f32_e32 v109, v107, v1
	v_mfma_f32_32x32x16_bf16 v[20:35], v[96:99], v[116:119], v[20:35]
	s_waitcnt vmcnt(8)
	v_mov_b32_e32 v104, v148
	v_mov_b32_e32 v105, v149
	v_mov_b32_e32 v106, v150
	v_mov_b32_e32 v107, v151
	v_and_b32_e32 v111, 0xffff0000, v104
	v_mfma_f32_32x32x16_bf16 v[20:35], v[100:103], v[116:119], v[20:35]
	v_lshlrev_b32_e32 v1, 16, v104
	v_mul_f32_e32 v111, v111, v111
	v_fmac_f32_e32 v111, v1, v1
	v_add_f32_e32 v1, v111, v109
	v_and_b32_e32 v111, 0xffff0000, v105
	v_lshlrev_b32_e32 v109, 16, v105
	v_mul_f32_e32 v111, v111, v111
	v_mfma_f32_32x32x16_bf16 v[20:35], v[92:95], v[104:107], v[20:35]
	v_fmac_f32_e32 v111, v109, v109
	v_add_f32_e32 v1, v111, v1
	v_and_b32_e32 v111, 0xffff0000, v106
	v_lshlrev_b32_e32 v109, 16, v106
	v_mul_f32_e32 v111, v111, v111
	v_fmac_f32_e32 v111, v109, v109
	v_add_f32_e32 v1, v111, v1
	v_mfma_f32_32x32x16_bf16 v[20:35], v[88:91], v[104:107], v[20:35]
	v_and_b32_e32 v111, 0xffff0000, v107
	v_lshlrev_b32_e32 v109, 16, v107
	v_mul_f32_e32 v111, v111, v111
	v_fmac_f32_e32 v111, v109, v109
	v_add_f32_e32 v109, v111, v1
	v_mov_b32_e32 v104, v109
	s_nop 1
	v_permlane32_swap_b32_e32 v109, v104
	s_and_saveexec_b64 s[4:5], vcc
	v_add_f32_e32 v1, v109, v104
	ds_write_b32 v2, v1
	s_or_b64 exec, exec, s[4:5]
	v_or_b32_e32 v1, s8, v114
	s_movk_i32 s2, 0x84
	v_mul_lo_u32 v1, v1, s2
	v_add_u32_e32 v1, 0, v1
	v_add_u32_e32 v104, v1, v108
	ds_write2_b32 v104, v20, v21 offset1:1
	ds_write2_b32 v104, v22, v23 offset0:2 offset1:3
	ds_write2_b32 v104, v24, v25 offset0:8 offset1:9
	ds_write2_b32 v104, v26, v27 offset0:10 offset1:11
	ds_write2_b32 v104, v28, v29 offset0:16 offset1:17
	ds_write2_b32 v104, v30, v31 offset0:18 offset1:19
	ds_write2_b32 v104, v32, v33 offset0:24 offset1:25
	ds_write2_b32 v104, v34, v35 offset0:26 offset1:27
	v_or_b32_e32 v20, 32, v110
	v_ashrrev_i32_e32 v21, 31, v20
	v_lshlrev_b64 v[20:21], 11, v[20:21]
	v_lshl_add_u64 v[16:17], v[16:17], 0, v[20:21]
	s_waitcnt vmcnt(7)
	v_mov_b32_e32 v106, v152
	v_mov_b32_e32 v107, v153
	v_mov_b32_e32 v108, v154
	v_mov_b32_e32 v109, v155
	v_and_b32_e32 v20, 0xffff0000, v106
	v_lshlrev_b32_e32 v1, 16, v106
	v_mul_f32_e32 v20, v20, v20
	v_and_b32_e32 v21, 0xffff0000, v107
	v_fmac_f32_e32 v20, v1, v1
	v_lshlrev_b32_e32 v1, 16, v107
	v_mul_f32_e32 v21, v21, v21
	v_fmac_f32_e32 v21, v1, v1
	v_add_f32_e32 v1, v20, v21
	v_and_b32_e32 v21, 0xffff0000, v108
	v_lshlrev_b32_e32 v20, 16, v108
	v_mul_f32_e32 v21, v21, v21
	v_fmac_f32_e32 v21, v20, v20
	v_add_f32_e32 v1, v21, v1
	v_and_b32_e32 v21, 0xffff0000, v109
	v_lshlrev_b32_e32 v20, 16, v109
	v_mul_f32_e32 v21, v21, v21
	v_fmac_f32_e32 v21, v20, v20
	v_add_f32_e32 v1, v21, v1
	v_mfma_f32_32x32x16_bf16 v[20:35], v[40:43], v[106:109], 0
	v_mfma_f32_32x32x16_bf16 v[20:35], v[44:47], v[106:109], v[20:35]
	s_waitcnt vmcnt(6)
	v_mov_b32_e32 v40, v156
	v_mov_b32_e32 v41, v157
	v_mov_b32_e32 v42, v158
	v_mov_b32_e32 v43, v159
	v_and_b32_e32 v45, 0xffff0000, v40
	v_lshlrev_b32_e32 v44, 16, v40
	v_mul_f32_e32 v45, v45, v45
	v_mfma_f32_32x32x16_bf16 v[20:35], v[48:51], v[40:43], v[20:35]
	v_fmac_f32_e32 v45, v44, v44
	v_add_f32_e32 v1, v1, v45
	v_and_b32_e32 v45, 0xffff0000, v41
	v_lshlrev_b32_e32 v44, 16, v41
	v_mul_f32_e32 v45, v45, v45
	v_fmac_f32_e32 v45, v44, v44
	v_add_f32_e32 v1, v45, v1
	v_and_b32_e32 v45, 0xffff0000, v42
	v_lshlrev_b32_e32 v44, 16, v42
	v_mul_f32_e32 v45, v45, v45
	v_fmac_f32_e32 v45, v44, v44
	v_add_f32_e32 v1, v45, v1
	v_lshlrev_b32_e32 v44, 16, v43
	v_and_b32_e32 v45, 0xffff0000, v43
	v_mfma_f32_32x32x16_bf16 v[20:35], v[52:55], v[40:43], v[20:35]
	v_mul_f32_e32 v45, v45, v45
	v_fmac_f32_e32 v45, v44, v44
	v_add_f32_e32 v1, v45, v1
	s_waitcnt vmcnt(5)
	v_mov_b32_e32 v40, v160
	v_mov_b32_e32 v41, v161
	v_mov_b32_e32 v42, v162
	v_mov_b32_e32 v43, v163
	v_and_b32_e32 v45, 0xffff0000, v40
	v_lshlrev_b32_e32 v44, 16, v40
	v_mul_f32_e32 v45, v45, v45
	v_mfma_f32_32x32x16_bf16 v[20:35], v[56:59], v[40:43], v[20:35]
	v_fmac_f32_e32 v45, v44, v44
	v_add_f32_e32 v1, v45, v1
	v_and_b32_e32 v45, 0xffff0000, v41
	v_lshlrev_b32_e32 v44, 16, v41
	v_mul_f32_e32 v45, v45, v45
	v_fmac_f32_e32 v45, v44, v44
	v_add_f32_e32 v1, v45, v1
	v_and_b32_e32 v45, 0xffff0000, v42
	v_lshlrev_b32_e32 v44, 16, v42
	v_mul_f32_e32 v45, v45, v45
	v_fmac_f32_e32 v45, v44, v44
	v_add_f32_e32 v1, v45, v1
	v_lshlrev_b32_e32 v44, 16, v43
	v_and_b32_e32 v45, 0xffff0000, v43
	v_mfma_f32_32x32x16_bf16 v[20:35], v[60:63], v[40:43], v[20:35]
	v_mul_f32_e32 v45, v45, v45
	v_fmac_f32_e32 v45, v44, v44
	v_add_f32_e32 v1, v45, v1
	s_waitcnt vmcnt(4)
	v_mov_b32_e32 v40, v164
	v_mov_b32_e32 v41, v165
	v_mov_b32_e32 v42, v166
	v_mov_b32_e32 v43, v167
	v_and_b32_e32 v45, 0xffff0000, v40
	v_lshlrev_b32_e32 v44, 16, v40
	v_mul_f32_e32 v45, v45, v45
	v_mfma_f32_32x32x16_bf16 v[20:35], v[64:67], v[40:43], v[20:35]
	v_fmac_f32_e32 v45, v44, v44
	v_add_f32_e32 v1, v45, v1
	v_and_b32_e32 v45, 0xffff0000, v41
	v_lshlrev_b32_e32 v44, 16, v41
	v_mul_f32_e32 v45, v45, v45
	v_fmac_f32_e32 v45, v44, v44
	v_add_f32_e32 v1, v45, v1
	v_and_b32_e32 v45, 0xffff0000, v42
	v_lshlrev_b32_e32 v44, 16, v42
	v_mul_f32_e32 v45, v45, v45
	v_fmac_f32_e32 v45, v44, v44
	v_add_f32_e32 v1, v45, v1
	v_lshlrev_b32_e32 v44, 16, v43
	v_and_b32_e32 v45, 0xffff0000, v43
	v_mfma_f32_32x32x16_bf16 v[20:35], v[68:71], v[40:43], v[20:35]
	v_mul_f32_e32 v45, v45, v45
	v_fmac_f32_e32 v45, v44, v44
	v_add_f32_e32 v1, v45, v1
	s_waitcnt vmcnt(3)
	v_mov_b32_e32 v40, v168
	v_mov_b32_e32 v41, v169
	v_mov_b32_e32 v42, v170
	v_mov_b32_e32 v43, v171
	v_and_b32_e32 v45, 0xffff0000, v40
	v_lshlrev_b32_e32 v44, 16, v40
	v_mul_f32_e32 v45, v45, v45
	v_mfma_f32_32x32x16_bf16 v[20:35], v[72:75], v[40:43], v[20:35]
	v_fmac_f32_e32 v45, v44, v44
	v_add_f32_e32 v1, v45, v1
	v_and_b32_e32 v45, 0xffff0000, v41
	v_lshlrev_b32_e32 v44, 16, v41
	v_mul_f32_e32 v45, v45, v45
	v_fmac_f32_e32 v45, v44, v44
	v_add_f32_e32 v1, v45, v1
	v_and_b32_e32 v45, 0xffff0000, v42
	v_lshlrev_b32_e32 v44, 16, v42
	v_mul_f32_e32 v45, v45, v45
	v_fmac_f32_e32 v45, v44, v44
	v_add_f32_e32 v1, v45, v1
	v_lshlrev_b32_e32 v44, 16, v43
	v_and_b32_e32 v45, 0xffff0000, v43
	v_mfma_f32_32x32x16_bf16 v[20:35], v[76:79], v[40:43], v[20:35]
	v_mul_f32_e32 v45, v45, v45
	v_fmac_f32_e32 v45, v44, v44
	v_add_f32_e32 v1, v45, v1
	s_waitcnt vmcnt(2)
	v_mov_b32_e32 v40, v172
	v_mov_b32_e32 v41, v173
	v_mov_b32_e32 v42, v174
	v_mov_b32_e32 v43, v175
	v_and_b32_e32 v45, 0xffff0000, v40
	v_lshlrev_b32_e32 v44, 16, v40
	v_mul_f32_e32 v45, v45, v45
	v_mfma_f32_32x32x16_bf16 v[20:35], v[80:83], v[40:43], v[20:35]
	v_fmac_f32_e32 v45, v44, v44
	v_add_f32_e32 v1, v45, v1
	v_and_b32_e32 v45, 0xffff0000, v41
	v_lshlrev_b32_e32 v44, 16, v41
	v_mul_f32_e32 v45, v45, v45
	v_fmac_f32_e32 v45, v44, v44
	v_add_f32_e32 v1, v45, v1
	v_and_b32_e32 v45, 0xffff0000, v42
	v_lshlrev_b32_e32 v44, 16, v42
	v_mul_f32_e32 v45, v45, v45
	v_fmac_f32_e32 v45, v44, v44
	v_add_f32_e32 v1, v45, v1
	v_lshlrev_b32_e32 v44, 16, v43
	v_and_b32_e32 v45, 0xffff0000, v43
	v_mfma_f32_32x32x16_bf16 v[20:35], v[84:87], v[40:43], v[20:35]
	v_mul_f32_e32 v45, v45, v45
	v_fmac_f32_e32 v45, v44, v44
	v_add_f32_e32 v1, v45, v1
	s_waitcnt vmcnt(1)
	v_mov_b32_e32 v40, v176
	v_mov_b32_e32 v41, v177
	v_mov_b32_e32 v42, v178
	v_mov_b32_e32 v43, v179
	v_and_b32_e32 v45, 0xffff0000, v40
	v_lshlrev_b32_e32 v44, 16, v40
	v_mul_f32_e32 v45, v45, v45
	v_mfma_f32_32x32x16_bf16 v[20:35], v[96:99], v[40:43], v[20:35]
	v_fmac_f32_e32 v45, v44, v44
	v_add_f32_e32 v1, v45, v1
	v_and_b32_e32 v45, 0xffff0000, v41
	v_lshlrev_b32_e32 v44, 16, v41
	v_mul_f32_e32 v45, v45, v45
	v_fmac_f32_e32 v45, v44, v44
	v_add_f32_e32 v1, v45, v1
	v_and_b32_e32 v45, 0xffff0000, v42
	v_lshlrev_b32_e32 v44, 16, v42
	v_mul_f32_e32 v45, v45, v45
	v_fmac_f32_e32 v45, v44, v44
	v_add_f32_e32 v1, v45, v1
	v_lshlrev_b32_e32 v44, 16, v43
	v_and_b32_e32 v45, 0xffff0000, v43
	v_mfma_f32_32x32x16_bf16 v[20:35], v[100:103], v[40:43], v[20:35]
	v_mul_f32_e32 v45, v45, v45
	v_fmac_f32_e32 v45, v44, v44
	v_add_f32_e32 v44, v45, v1
	s_waitcnt vmcnt(0)
	v_mov_b32_e32 v40, v180
	v_mov_b32_e32 v41, v181
	v_mov_b32_e32 v42, v182
	v_mov_b32_e32 v43, v183
	v_and_b32_e32 v16, 0xffff0000, v40
	v_mfma_f32_32x32x16_bf16 v[20:35], v[92:95], v[40:43], v[20:35]
	v_lshlrev_b32_e32 v1, 16, v40
	v_mul_f32_e32 v16, v16, v16
	v_fmac_f32_e32 v16, v1, v1
	v_and_b32_e32 v17, 0xffff0000, v41
	v_add_f32_e32 v1, v16, v44
	v_lshlrev_b32_e32 v16, 16, v41
	v_mul_f32_e32 v17, v17, v17
	v_fmac_f32_e32 v17, v16, v16
	v_add_f32_e32 v1, v17, v1
	v_and_b32_e32 v17, 0xffff0000, v42
	v_lshlrev_b32_e32 v16, 16, v42
	v_mul_f32_e32 v17, v17, v17
	v_mfma_f32_32x32x16_bf16 v[20:35], v[88:91], v[40:43], v[20:35]
	v_fmac_f32_e32 v17, v16, v16
	v_add_f32_e32 v1, v17, v1
	v_and_b32_e32 v17, 0xffff0000, v43
	v_lshlrev_b32_e32 v16, 16, v43
	v_mul_f32_e32 v17, v17, v17
	v_fmac_f32_e32 v17, v16, v16
	v_add_f32_e32 v16, v17, v1
	v_mov_b32_e32 v17, v16
	s_nop 1
	v_permlane32_swap_b32_e32 v16, v17
	s_and_saveexec_b64 s[4:5], vcc
	v_add_f32_e32 v1, v16, v17
	ds_write_b32 v2, v1 offset:128
	s_or_b64 exec, exec, s[4:5]
	v_add_u32_e32 v1, 0x1080, v104
	ds_write2_b32 v1, v20, v21 offset1:1
	v_add_u32_e32 v1, 0x1088, v104
	ds_write2_b32 v1, v22, v23 offset1:1
	v_add_u32_e32 v1, 0x10a0, v104
	ds_write2_b32 v1, v24, v25 offset1:1
	v_add_u32_e32 v1, 0x10a8, v104
	ds_write2_b32 v1, v26, v27 offset1:1
	v_add_u32_e32 v1, 0x10c0, v104
	ds_write2_b32 v1, v28, v29 offset1:1
	v_add_u32_e32 v1, 0x10c8, v104
	ds_write2_b32 v1, v30, v31 offset1:1
	v_add_u32_e32 v1, 0x10e0, v104
	ds_write2_b32 v1, v32, v33 offset1:1
	v_add_u32_e32 v1, 0x10e8, v104
	v_readlane_b32 s2, v255, 4
	ds_write2_b32 v1, v34, v35 offset1:1
	v_ashrrev_i32_e32 v1, 3, v19
	s_lshl_b32 s82, s2, 5
	s_mov_b32 s83, s73
	v_lshl_add_u32 v2, v1, 2, 0
	s_lshl_b64 s[2:3], s[82:83], 2
	v_add_u32_e32 v2, 0x10800, v2
	s_waitcnt lgkmcnt(0)
	s_add_u32 s0, s0, s2
	s_barrier
	ds_read2st64_b32 v[16:17], v2 offset1:1
	ds_read2st64_b32 v[20:21], v2 offset0:2 offset1:3
	ds_read2st64_b32 v[22:23], v2 offset0:4 offset1:5
	ds_read2st64_b32 v[28:29], v2 offset0:6 offset1:7
	v_lshlrev_b32_e32 v2, 4, v19
	s_addc_u32 s1, s1, s3
	v_and_b32_e32 v30, 0x70, v2
	global_load_dwordx4 v[24:27], v30, s[0:1]
	s_waitcnt lgkmcnt(3)
	v_add_f32_e32 v2, 0, v16
	v_add_f32_e32 v2, v2, v17
	s_waitcnt lgkmcnt(2)
	v_add_f32_e32 v2, v2, v20
	v_add_f32_e32 v2, v2, v21
	s_waitcnt lgkmcnt(1)
	v_add_f32_e32 v2, v2, v22
	v_add_f32_e32 v2, v2, v23
	s_waitcnt lgkmcnt(0)
	v_add_f32_e32 v2, v2, v28
	v_add_f32_e32 v2, v2, v29
	v_fmamk_f32 v2, v2, 0x3a800000, v220
	v_mul_f32_e32 v16, 0x4f800000, v2
	v_cmp_gt_f32_e32 vcc, s93, v2
	v_mov_b32_e32 v23, 0
	v_cmp_gt_i32_e64 s[8:9], 64, v19
	v_cndmask_b32_e32 v2, v2, v16, vcc
	v_sqrt_f32_e32 v16, v2
	v_mov_b32_e32 v56, 0
	v_mov_b32_e32 v54, 0
	v_add_u32_e32 v17, -1, v16
	v_fma_f32 v20, -v17, v16, v2
	v_cmp_ge_f32_e64 s[0:1], 0, v20
	v_add_u32_e32 v20, 1, v16
	s_nop 0
	v_cndmask_b32_e64 v17, v16, v17, s[0:1]
	v_fma_f32 v16, -v20, v16, v2
	v_cmp_lt_f32_e64 s[0:1], 0, v16
	s_nop 1
	v_cndmask_b32_e64 v16, v17, v20, s[0:1]
	v_mul_f32_e32 v17, 0x37800000, v16
	v_cndmask_b32_e32 v16, v16, v17, vcc
	v_cmp_class_f32_e32 vcc, v2, v221
	s_nop 1
	v_cndmask_b32_e32 v2, v16, v2, vcc
	v_div_scale_f32 v16, s[0:1], v2, v2, 1.0
	v_rcp_f32_e32 v17, v16
	s_movk_i32 s0, 0x84
	v_mul_lo_u32 v1, v1, s0
	s_add_i32 s0, 0, 0x20400
	v_fma_f32 v20, -v16, v17, 1.0
	v_fmac_f32_e32 v17, v20, v17
	v_div_scale_f32 v20, vcc, 1.0, v2, 1.0
	v_mul_f32_e32 v21, v20, v17
	v_fma_f32 v22, -v16, v21, v20
	v_fmac_f32_e32 v21, v22, v17
	v_fma_f32 v16, -v16, v21, v20
	v_add3_u32 v22, s0, v1, v30
	v_add3_u32 v1, 0, v30, v1
	v_div_fmas_f32 v16, v16, v17, v21
	v_add_u32_e32 v20, 0x2100, v1
	v_div_fixup_f32 v2, v16, v2, 1.0
	ds_read2_b32 v[16:17], v1 offset1:1
	ds_read2_b32 v[20:21], v20 offset1:1
	v_add_u32_e32 v28, 0x4200, v1
	ds_read2_b32 v[28:29], v28 offset1:1
	ds_read2_b32 v[30:31], v1 offset0:2 offset1:3
	v_add_u32_e32 v32, 0x6300, v1
	v_add_u32_e32 v33, 0x8400, v1
	v_add_u32_e32 v34, 0xa500, v1
	v_add_u32_e32 v40, 0xc600, v1
	s_waitcnt lgkmcnt(3)
	v_pk_add_f32 v[16:17], v[16:17], 0 op_sel_hi:[1,0]
	v_add_u32_e32 v42, 0xe700, v1
	s_waitcnt lgkmcnt(2)
	v_pk_add_f32 v[16:17], v[16:17], v[20:21]
	ds_read2_b32 v[20:21], v32 offset1:1
	ds_read2_b32 v[32:33], v33 offset1:1
	ds_read2_b32 v[34:35], v34 offset1:1
	ds_read2_b32 v[40:41], v40 offset1:1
	s_waitcnt lgkmcnt(5)
	v_pk_add_f32 v[16:17], v[16:17], v[28:29]
	v_add_u32_e32 v28, 0x2108, v1
	s_waitcnt lgkmcnt(3)
	v_pk_add_f32 v[16:17], v[16:17], v[20:21]
	ds_read2_b32 v[20:21], v42 offset1:1
	s_waitcnt lgkmcnt(3)
	v_pk_add_f32 v[16:17], v[16:17], v[32:33]
	v_add_u32_e32 v32, 0x4208, v1
	s_waitcnt lgkmcnt(2)
	v_pk_add_f32 v[16:17], v[16:17], v[34:35]
	v_add_u32_e32 v34, 0x6308, v1
	s_waitcnt lgkmcnt(1)
	v_pk_add_f32 v[16:17], v[16:17], v[40:41]
	ds_read2_b32 v[28:29], v28 offset1:1
	ds_read2_b32 v[32:33], v32 offset1:1
	ds_read2_b32 v[34:35], v34 offset1:1
	s_waitcnt lgkmcnt(3)
	v_pk_add_f32 v[16:17], v[16:17], v[20:21]
	v_add_u32_e32 v20, 0x8408, v1
	v_add_u32_e32 v40, 0xc608, v1
	s_waitcnt vmcnt(0)
	v_pk_fma_f32 v[16:17], v[2:3], v[16:17], v[24:25] op_sel_hi:[0,1,1]
	ds_write2_b32 v22, v16, v17 offset1:1
	v_pk_add_f32 v[16:17], v[30:31], 0 op_sel_hi:[1,0]
	v_add_u32_e32 v24, 0xa508, v1
	s_waitcnt lgkmcnt(3)
	v_pk_add_f32 v[16:17], v[16:17], v[28:29]
	v_add_u32_e32 v1, 0xe708, v1
	s_waitcnt lgkmcnt(2)
	v_pk_add_f32 v[16:17], v[16:17], v[32:33]
	ds_read2_b32 v[20:21], v20 offset1:1
	ds_read2_b32 v[24:25], v24 offset1:1
	ds_read2_b32 v[28:29], v40 offset1:1
	ds_read2_b32 v[30:31], v1 offset1:1
	s_waitcnt lgkmcnt(5)
	v_pk_add_f32 v[16:17], v[16:17], v[34:35]
	s_waitcnt lgkmcnt(3)
	v_pk_add_f32 v[16:17], v[16:17], v[20:21]
	v_mov_b32_e32 v20, 0
	s_waitcnt lgkmcnt(2)
	v_pk_add_f32 v[16:17], v[16:17], v[24:25]
	v_mov_b32_e32 v25, 0
	s_waitcnt lgkmcnt(1)
	v_pk_add_f32 v[16:17], v[16:17], v[28:29]
	v_mov_b32_e32 v21, 0
	s_waitcnt lgkmcnt(0)
	v_pk_add_f32 v[16:17], v[16:17], v[30:31]
	v_mov_b32_e32 v24, 0
	v_pk_fma_f32 v[16:17], v[2:3], v[16:17], v[26:27] op_sel_hi:[0,1,1]
	ds_write2_b32 v22, v16, v17 offset0:2 offset1:3
	v_mov_b32_e32 v26, 0
	v_mov_b32_e32 v22, 0
	v_mov_b32_e32 v2, 0
	v_mov_b32_e32 v16, 0
	v_mov_b32_e32 v17, 0
	s_waitcnt lgkmcnt(0)
	s_barrier
	s_and_saveexec_b64 s[84:85], s[8:9]
	s_cbranch_execz .LBB0_1749
	s_movk_i32 s0, 0x84
	v_mul_lo_u32 v1, v19, s0
	v_add_u32_e32 v1, 0, v1
	v_add_u32_e32 v1, 0x20400, v1
	s_mov_b32 s0, 0xff800000
	ds_read2_b32 v[52:53], v1 offset1:1
	ds_read2_b32 v[50:51], v1 offset0:2 offset1:3
	ds_read2_b32 v[48:49], v1 offset0:4 offset1:5
	ds_read2_b32 v[46:47], v1 offset0:6 offset1:7
	ds_read2_b32 v[44:45], v1 offset0:8 offset1:9
	ds_read2_b32 v[42:43], v1 offset0:10 offset1:11
	ds_read2_b32 v[40:41], v1 offset0:12 offset1:13
	ds_read2_b32 v[34:35], v1 offset0:14 offset1:15
	ds_read2_b32 v[32:33], v1 offset0:16 offset1:17
	ds_read2_b32 v[30:31], v1 offset0:18 offset1:19
	ds_read2_b32 v[28:29], v1 offset0:20 offset1:21
	ds_read2_b32 v[26:27], v1 offset0:22 offset1:23
	ds_read2_b32 v[24:25], v1 offset0:24 offset1:25
	ds_read2_b32 v[22:23], v1 offset0:26 offset1:27
	ds_read2_b32 v[20:21], v1 offset0:28 offset1:29
	ds_read2_b32 v[16:17], v1 offset0:30 offset1:31
	s_waitcnt lgkmcnt(14)
	v_cmp_lg_f32_e32 vcc, s0, v52
	v_cmp_nlg_f32_e64 s[0:1], s0, v52
	s_nop 0
	v_cndmask_b32_e32 v1, v18, v52, vcc
	v_cmp_gt_f32_e32 vcc, v53, v1
	s_nop 1
	v_cndmask_b32_e32 v1, v1, v53, vcc
	v_cndmask_b32_e64 v2, 0, 1, vcc
	v_cmp_gt_f32_e32 vcc, v50, v1
	s_nop 1
	v_cndmask_b32_e32 v1, v1, v50, vcc
	v_cndmask_b32_e64 v2, v2, 2, vcc
	v_cmp_gt_f32_e32 vcc, v51, v1
	s_nop 1
	v_cndmask_b32_e32 v1, v1, v51, vcc
	v_cndmask_b32_e64 v2, v2, 3, vcc
	s_waitcnt lgkmcnt(13)
	v_cmp_gt_f32_e32 vcc, v48, v1
	s_nop 1
	v_cndmask_b32_e32 v1, v1, v48, vcc
	v_cndmask_b32_e64 v2, v2, 4, vcc
	v_cmp_gt_f32_e32 vcc, v49, v1
	s_nop 1
	v_cndmask_b32_e32 v1, v1, v49, vcc
	v_cndmask_b32_e64 v2, v2, 5, vcc
	s_waitcnt lgkmcnt(12)
	v_cmp_gt_f32_e32 vcc, v46, v1
	s_nop 1
	v_cndmask_b32_e32 v1, v1, v46, vcc
	v_cndmask_b32_e64 v2, v2, 6, vcc
	v_cmp_gt_f32_e32 vcc, v47, v1
	s_nop 1
	v_cndmask_b32_e32 v1, v1, v47, vcc
	v_cndmask_b32_e64 v2, v2, 7, vcc
	s_waitcnt lgkmcnt(11)
	v_cmp_gt_f32_e32 vcc, v44, v1
	s_nop 1
	v_cndmask_b32_e32 v1, v1, v44, vcc
	v_cndmask_b32_e64 v2, v2, 8, vcc
	v_cmp_gt_f32_e32 vcc, v45, v1
	s_nop 1
	v_cndmask_b32_e32 v1, v1, v45, vcc
	v_cndmask_b32_e64 v2, v2, 9, vcc
	s_waitcnt lgkmcnt(10)
	v_cmp_gt_f32_e32 vcc, v42, v1
	s_nop 1
	v_cndmask_b32_e32 v1, v1, v42, vcc
	v_cndmask_b32_e64 v2, v2, 10, vcc
	v_cmp_gt_f32_e32 vcc, v43, v1
	s_nop 1
	v_cndmask_b32_e32 v1, v1, v43, vcc
	v_cndmask_b32_e64 v2, v2, 11, vcc
	s_waitcnt lgkmcnt(9)
	v_cmp_gt_f32_e32 vcc, v40, v1
	s_nop 1
	v_cndmask_b32_e32 v1, v1, v40, vcc
	v_cndmask_b32_e64 v2, v2, 12, vcc
	v_cmp_gt_f32_e32 vcc, v41, v1
	s_nop 1
	v_cndmask_b32_e32 v1, v1, v41, vcc
	v_cndmask_b32_e64 v2, v2, 13, vcc
	s_waitcnt lgkmcnt(8)
	v_cmp_gt_f32_e32 vcc, v34, v1
	s_nop 1
	v_cndmask_b32_e32 v1, v1, v34, vcc
	v_cndmask_b32_e64 v2, v2, 14, vcc
	v_cmp_gt_f32_e32 vcc, v35, v1
	s_nop 1
	v_cndmask_b32_e32 v1, v1, v35, vcc
	v_cndmask_b32_e64 v2, v2, 15, vcc
	s_waitcnt lgkmcnt(7)
	v_cmp_gt_f32_e32 vcc, v32, v1
	s_nop 1
	v_cndmask_b32_e32 v1, v1, v32, vcc
	v_cndmask_b32_e64 v2, v2, 16, vcc
	v_cmp_gt_f32_e32 vcc, v33, v1
	s_nop 1
	v_cndmask_b32_e32 v1, v1, v33, vcc
	v_cndmask_b32_e64 v2, v2, 17, vcc
	s_waitcnt lgkmcnt(6)
	v_cmp_gt_f32_e32 vcc, v30, v1
	s_nop 1
	v_cndmask_b32_e32 v1, v1, v30, vcc
	v_cndmask_b32_e64 v2, v2, 18, vcc
	v_cmp_gt_f32_e32 vcc, v31, v1
	s_nop 1
	v_cndmask_b32_e32 v1, v1, v31, vcc
	v_cndmask_b32_e64 v2, v2, 19, vcc
	s_waitcnt lgkmcnt(5)
	v_cmp_gt_f32_e32 vcc, v28, v1
	s_nop 1
	v_cndmask_b32_e32 v1, v1, v28, vcc
	v_cndmask_b32_e64 v2, v2, 20, vcc
	v_cmp_gt_f32_e32 vcc, v29, v1
	s_nop 1
	v_cndmask_b32_e32 v1, v1, v29, vcc
	v_cndmask_b32_e64 v2, v2, 21, vcc
	s_waitcnt lgkmcnt(4)
	v_cmp_gt_f32_e32 vcc, v26, v1
	s_nop 1
	v_cndmask_b32_e32 v1, v1, v26, vcc
	v_cndmask_b32_e64 v2, v2, 22, vcc
	v_cmp_gt_f32_e32 vcc, v27, v1
	s_nop 1
	v_cndmask_b32_e32 v1, v1, v27, vcc
	v_cndmask_b32_e64 v2, v2, 23, vcc
	s_waitcnt lgkmcnt(3)
	v_cmp_gt_f32_e32 vcc, v24, v1
	s_nop 1
	v_cndmask_b32_e32 v1, v1, v24, vcc
	v_cndmask_b32_e64 v2, v2, 24, vcc
	v_cmp_gt_f32_e32 vcc, v25, v1
	s_nop 1
	v_cndmask_b32_e32 v1, v1, v25, vcc
	v_cndmask_b32_e64 v2, v2, 25, vcc
	s_waitcnt lgkmcnt(2)
	v_cmp_gt_f32_e32 vcc, v22, v1
	s_nop 1
	v_cndmask_b32_e32 v1, v1, v22, vcc
	v_cndmask_b32_e64 v2, v2, 26, vcc
	v_cmp_gt_f32_e32 vcc, v23, v1
	s_nop 1
	v_cndmask_b32_e32 v1, v1, v23, vcc
	v_cndmask_b32_e64 v2, v2, 27, vcc
	s_waitcnt lgkmcnt(1)
	v_cmp_gt_f32_e32 vcc, v20, v1
	s_nop 1
	v_cndmask_b32_e32 v1, v1, v20, vcc
	v_cndmask_b32_e64 v2, v2, 28, vcc
	v_cmp_gt_f32_e32 vcc, v21, v1
	s_nop 1
	v_cndmask_b32_e32 v1, v1, v21, vcc
	v_cndmask_b32_e64 v2, v2, 29, vcc
	s_waitcnt lgkmcnt(0)
	v_cmp_gt_f32_e32 vcc, v16, v1
	s_nop 1
	v_cndmask_b32_e32 v1, v1, v16, vcc
	v_cndmask_b32_e64 v2, v2, 30, vcc
	v_cmp_gt_f32_e32 vcc, v17, v1
	s_nop 1
	v_cndmask_b32_e64 v2, v2, 31, vcc
	v_cndmask_b32_e32 v55, v1, v17, vcc
	v_cmp_eq_u32_e32 vcc, 0, v2
	s_or_b64 s[0:1], vcc, s[0:1]
	v_cndmask_b32_e64 v1, v52, v18, s[0:1]
	v_cmp_ne_u32_e64 s[66:67], 1, v2
	v_cmp_gt_f32_e32 vcc, v53, v1
	s_and_b64 vcc, s[66:67], vcc
	v_cmp_ne_u32_e64 s[64:65], 2, v2
	v_cndmask_b32_e32 v1, v1, v53, vcc
	v_cndmask_b32_e64 v54, 0, 1, vcc
	v_cmp_gt_f32_e32 vcc, v50, v1
	s_and_b64 vcc, s[64:65], vcc
	v_cmp_ne_u32_e64 s[62:63], 3, v2
	v_cndmask_b32_e32 v1, v1, v50, vcc
	v_cndmask_b32_e64 v54, v54, 2, vcc
	v_cmp_gt_f32_e32 vcc, v51, v1
	s_and_b64 vcc, s[62:63], vcc
	v_cmp_ne_u32_e64 s[60:61], 4, v2
	v_cndmask_b32_e32 v1, v1, v51, vcc
	v_cndmask_b32_e64 v54, v54, 3, vcc
	v_cmp_gt_f32_e32 vcc, v48, v1
	s_and_b64 vcc, s[60:61], vcc
	v_cmp_ne_u32_e64 s[58:59], 5, v2
	v_cndmask_b32_e32 v1, v1, v48, vcc
	v_cndmask_b32_e64 v54, v54, 4, vcc
	v_cmp_gt_f32_e32 vcc, v49, v1
	s_and_b64 vcc, s[58:59], vcc
	v_cmp_ne_u32_e64 s[56:57], 6, v2
	v_cndmask_b32_e32 v1, v1, v49, vcc
	v_cndmask_b32_e64 v54, v54, 5, vcc
	v_cmp_gt_f32_e32 vcc, v46, v1
	s_and_b64 vcc, s[56:57], vcc
	v_cmp_ne_u32_e64 s[54:55], 7, v2
	v_cndmask_b32_e32 v1, v1, v46, vcc
	v_cndmask_b32_e64 v54, v54, 6, vcc
	v_cmp_gt_f32_e32 vcc, v47, v1
	s_and_b64 vcc, s[54:55], vcc
	v_cmp_ne_u32_e64 s[52:53], 8, v2
	v_cndmask_b32_e32 v1, v1, v47, vcc
	v_cndmask_b32_e64 v54, v54, 7, vcc
	v_cmp_gt_f32_e32 vcc, v44, v1
	s_and_b64 vcc, s[52:53], vcc
	v_cmp_ne_u32_e64 s[50:51], 9, v2
	v_cndmask_b32_e32 v1, v1, v44, vcc
	v_cndmask_b32_e64 v54, v54, 8, vcc
	v_cmp_gt_f32_e32 vcc, v45, v1
	s_and_b64 vcc, s[50:51], vcc
	v_cmp_ne_u32_e64 s[48:49], 10, v2
	v_cndmask_b32_e32 v1, v1, v45, vcc
	v_cndmask_b32_e64 v54, v54, 9, vcc
	v_cmp_gt_f32_e32 vcc, v42, v1
	s_and_b64 vcc, s[48:49], vcc
	v_cmp_ne_u32_e64 s[46:47], 11, v2
	v_cndmask_b32_e32 v1, v1, v42, vcc
	v_cndmask_b32_e64 v54, v54, 10, vcc
	v_cmp_gt_f32_e32 vcc, v43, v1
	s_and_b64 vcc, s[46:47], vcc
	v_cmp_ne_u32_e64 s[44:45], 12, v2
	v_cndmask_b32_e32 v1, v1, v43, vcc
	v_cndmask_b32_e64 v54, v54, 11, vcc
	v_cmp_gt_f32_e32 vcc, v40, v1
	s_and_b64 vcc, s[44:45], vcc
	v_cmp_ne_u32_e64 s[42:43], 13, v2
	v_cndmask_b32_e32 v1, v1, v40, vcc
	v_cndmask_b32_e64 v54, v54, 12, vcc
	v_cmp_gt_f32_e32 vcc, v41, v1
	s_and_b64 vcc, s[42:43], vcc
	v_cmp_ne_u32_e64 s[40:41], 14, v2
	v_cndmask_b32_e32 v1, v1, v41, vcc
	v_cndmask_b32_e64 v54, v54, 13, vcc
	v_cmp_gt_f32_e32 vcc, v34, v1
	s_and_b64 vcc, s[40:41], vcc
	v_cmp_ne_u32_e64 s[38:39], 15, v2
	v_cndmask_b32_e32 v1, v1, v34, vcc
	v_cndmask_b32_e64 v54, v54, 14, vcc
	v_cmp_gt_f32_e32 vcc, v35, v1
	s_and_b64 vcc, s[38:39], vcc
	v_cmp_ne_u32_e64 s[36:37], 16, v2
	v_cndmask_b32_e32 v1, v1, v35, vcc
	v_cndmask_b32_e64 v54, v54, 15, vcc
	v_cmp_gt_f32_e32 vcc, v32, v1
	s_and_b64 vcc, s[36:37], vcc
	v_cmp_ne_u32_e64 s[34:35], 17, v2
	v_cndmask_b32_e32 v1, v1, v32, vcc
	v_cndmask_b32_e64 v54, v54, 16, vcc
	v_cmp_gt_f32_e32 vcc, v33, v1
	s_and_b64 vcc, s[34:35], vcc
	v_cmp_ne_u32_e64 s[30:31], 18, v2
	v_cndmask_b32_e32 v1, v1, v33, vcc
	v_cndmask_b32_e64 v54, v54, 17, vcc
	v_cmp_gt_f32_e32 vcc, v30, v1
	s_and_b64 vcc, s[30:31], vcc
	v_cmp_ne_u32_e64 s[28:29], 19, v2
	v_cndmask_b32_e32 v1, v1, v30, vcc
	v_cndmask_b32_e64 v54, v54, 18, vcc
	v_cmp_gt_f32_e32 vcc, v31, v1
	s_and_b64 vcc, s[28:29], vcc
	v_cmp_ne_u32_e64 s[26:27], 20, v2
	v_cndmask_b32_e32 v1, v1, v31, vcc
	v_cndmask_b32_e64 v54, v54, 19, vcc
	v_cmp_gt_f32_e32 vcc, v28, v1
	s_and_b64 vcc, s[26:27], vcc
	v_cmp_ne_u32_e64 s[24:25], 21, v2
	v_cndmask_b32_e32 v1, v1, v28, vcc
	v_cndmask_b32_e64 v54, v54, 20, vcc
	v_cmp_gt_f32_e32 vcc, v29, v1
	s_and_b64 vcc, s[24:25], vcc
	v_cmp_ne_u32_e64 s[22:23], 22, v2
	v_cndmask_b32_e32 v1, v1, v29, vcc
	v_cndmask_b32_e64 v54, v54, 21, vcc
	v_cmp_gt_f32_e32 vcc, v26, v1
	s_and_b64 vcc, s[22:23], vcc
	v_cmp_ne_u32_e64 s[20:21], 23, v2
	v_cndmask_b32_e32 v1, v1, v26, vcc
	v_cndmask_b32_e64 v54, v54, 22, vcc
	v_cmp_gt_f32_e32 vcc, v27, v1
	s_and_b64 vcc, s[20:21], vcc
	v_cmp_ne_u32_e64 s[18:19], 24, v2
	v_cndmask_b32_e32 v1, v1, v27, vcc
	v_cndmask_b32_e64 v54, v54, 23, vcc
	v_cmp_gt_f32_e32 vcc, v24, v1
	s_and_b64 vcc, s[18:19], vcc
	v_cmp_ne_u32_e64 s[16:17], 25, v2
	v_cndmask_b32_e32 v1, v1, v24, vcc
	v_cndmask_b32_e64 v54, v54, 24, vcc
	v_cmp_gt_f32_e32 vcc, v25, v1
	s_and_b64 vcc, s[16:17], vcc
	v_cmp_ne_u32_e64 s[14:15], 26, v2
	v_cndmask_b32_e32 v1, v1, v25, vcc
	v_cndmask_b32_e64 v54, v54, 25, vcc
	v_cmp_gt_f32_e32 vcc, v22, v1
	s_and_b64 vcc, s[14:15], vcc
	v_cmp_ne_u32_e64 s[12:13], 27, v2
	v_cndmask_b32_e32 v1, v1, v22, vcc
	v_cndmask_b32_e64 v54, v54, 26, vcc
	v_cmp_gt_f32_e32 vcc, v23, v1
	s_and_b64 vcc, s[12:13], vcc
	v_cmp_ne_u32_e64 s[10:11], 28, v2
	v_cndmask_b32_e32 v1, v1, v23, vcc
	v_cndmask_b32_e64 v54, v54, 27, vcc
	v_cmp_gt_f32_e32 vcc, v20, v1
	s_and_b64 vcc, s[10:11], vcc
	v_cmp_ne_u32_e64 s[4:5], 29, v2
	v_cndmask_b32_e32 v1, v1, v20, vcc
	v_cndmask_b32_e64 v54, v54, 28, vcc
	v_cmp_gt_f32_e32 vcc, v21, v1
	s_and_b64 vcc, s[4:5], vcc
	v_cmp_ne_u32_e64 s[74:75], 30, v2
	v_cndmask_b32_e32 v1, v1, v21, vcc
	v_cndmask_b32_e64 v54, v54, 29, vcc
	v_cmp_gt_f32_e32 vcc, v16, v1
	s_and_b64 vcc, s[74:75], vcc
	s_nop 0
	v_cndmask_b32_e32 v1, v1, v16, vcc
	v_cndmask_b32_e64 v54, v54, 30, vcc
	v_cmp_ne_u32_e32 vcc, 31, v2
	v_cmp_gt_f32_e64 s[70:71], v17, v1
	s_and_b64 s[70:71], vcc, s[70:71]
	s_nop 0
	v_cndmask_b32_e64 v54, v54, 31, s[70:71]
	v_cndmask_b32_e64 v1, v1, v17, s[70:71]
	v_cmp_eq_u32_e64 s[70:71], 0, v54
	s_or_b64 s[0:1], s[0:1], s[70:71]
	v_cndmask_b32_e64 v56, v52, v18, s[0:1]
	v_cmp_ne_u32_e64 s[70:71], 1, v54
	s_and_b64 s[70:71], s[66:67], s[70:71]
	v_cmp_gt_f32_e64 s[66:67], v53, v56
	s_and_b64 s[66:67], s[70:71], s[66:67]
	v_sub_f32_e32 v1, v1, v55
	v_cndmask_b32_e64 v56, v56, v53, s[66:67]
	v_cndmask_b32_e64 v57, 0, 1, s[66:67]
	v_cmp_ne_u32_e64 s[66:67], 2, v54
	s_and_b64 s[66:67], s[64:65], s[66:67]
	v_cmp_gt_f32_e64 s[64:65], v50, v56
	s_and_b64 s[64:65], s[66:67], s[64:65]
	v_mul_f32_e32 v1, 0x3fb8aa3b, v1
	v_cndmask_b32_e64 v56, v56, v50, s[64:65]
	v_cndmask_b32_e64 v57, v57, 2, s[64:65]
	v_cmp_ne_u32_e64 s[64:65], 3, v54
	s_and_b64 s[64:65], s[62:63], s[64:65]
	v_cmp_gt_f32_e64 s[62:63], v51, v56
	s_and_b64 s[62:63], s[64:65], s[62:63]
	s_nop 0
	v_cndmask_b32_e64 v56, v56, v51, s[62:63]
	v_cndmask_b32_e64 v57, v57, 3, s[62:63]
	v_cmp_ne_u32_e64 s[62:63], 4, v54
	s_and_b64 s[62:63], s[60:61], s[62:63]
	v_cmp_gt_f32_e64 s[60:61], v48, v56
	s_and_b64 s[60:61], s[62:63], s[60:61]
	s_nop 0
	v_cndmask_b32_e64 v56, v56, v48, s[60:61]
	v_cndmask_b32_e64 v57, v57, 4, s[60:61]
	v_cmp_ne_u32_e64 s[60:61], 5, v54
	s_and_b64 s[60:61], s[58:59], s[60:61]
	v_cmp_gt_f32_e64 s[58:59], v49, v56
	s_and_b64 s[58:59], s[60:61], s[58:59]
	s_nop 0
	v_cndmask_b32_e64 v56, v56, v49, s[58:59]
	v_cndmask_b32_e64 v57, v57, 5, s[58:59]
	v_cmp_ne_u32_e64 s[58:59], 6, v54
	s_and_b64 s[58:59], s[56:57], s[58:59]
	v_cmp_gt_f32_e64 s[56:57], v46, v56
	s_and_b64 s[56:57], s[58:59], s[56:57]
	s_nop 0
	v_cndmask_b32_e64 v56, v56, v46, s[56:57]
	v_cndmask_b32_e64 v57, v57, 6, s[56:57]
	v_cmp_ne_u32_e64 s[56:57], 7, v54
	s_and_b64 s[56:57], s[54:55], s[56:57]
	v_cmp_gt_f32_e64 s[54:55], v47, v56
	s_and_b64 s[54:55], s[56:57], s[54:55]
	s_nop 0
	v_cndmask_b32_e64 v56, v56, v47, s[54:55]
	v_cndmask_b32_e64 v57, v57, 7, s[54:55]
	v_cmp_ne_u32_e64 s[54:55], 8, v54
	s_and_b64 s[54:55], s[52:53], s[54:55]
	v_cmp_gt_f32_e64 s[52:53], v44, v56
	s_and_b64 s[52:53], s[54:55], s[52:53]
	s_nop 0
	v_cndmask_b32_e64 v56, v56, v44, s[52:53]
	v_cndmask_b32_e64 v57, v57, 8, s[52:53]
	v_cmp_ne_u32_e64 s[52:53], 9, v54
	s_and_b64 s[52:53], s[50:51], s[52:53]
	v_cmp_gt_f32_e64 s[50:51], v45, v56
	s_and_b64 s[50:51], s[52:53], s[50:51]
	s_nop 0
	v_cndmask_b32_e64 v56, v56, v45, s[50:51]
	v_cndmask_b32_e64 v57, v57, 9, s[50:51]
	v_cmp_ne_u32_e64 s[50:51], 10, v54
	s_and_b64 s[50:51], s[48:49], s[50:51]
	v_cmp_gt_f32_e64 s[48:49], v42, v56
	s_and_b64 s[48:49], s[50:51], s[48:49]
	s_nop 0
	v_cndmask_b32_e64 v56, v56, v42, s[48:49]
	v_cndmask_b32_e64 v57, v57, 10, s[48:49]
	v_cmp_ne_u32_e64 s[48:49], 11, v54
	s_and_b64 s[48:49], s[46:47], s[48:49]
	v_cmp_gt_f32_e64 s[46:47], v43, v56
	s_and_b64 s[46:47], s[48:49], s[46:47]
	s_nop 0
	v_cndmask_b32_e64 v56, v56, v43, s[46:47]
	v_cndmask_b32_e64 v57, v57, 11, s[46:47]
	v_cmp_ne_u32_e64 s[46:47], 12, v54
	s_and_b64 s[46:47], s[44:45], s[46:47]
	v_cmp_gt_f32_e64 s[44:45], v40, v56
	s_and_b64 s[44:45], s[46:47], s[44:45]
	s_nop 0
	v_cndmask_b32_e64 v56, v56, v40, s[44:45]
	v_cndmask_b32_e64 v57, v57, 12, s[44:45]
	v_cmp_ne_u32_e64 s[44:45], 13, v54
	s_and_b64 s[44:45], s[42:43], s[44:45]
	v_cmp_gt_f32_e64 s[42:43], v41, v56
	s_and_b64 s[42:43], s[44:45], s[42:43]
	s_nop 0
	v_cndmask_b32_e64 v56, v56, v41, s[42:43]
	v_cndmask_b32_e64 v57, v57, 13, s[42:43]
	v_cmp_ne_u32_e64 s[42:43], 14, v54
	s_and_b64 s[42:43], s[40:41], s[42:43]
	v_cmp_gt_f32_e64 s[40:41], v34, v56
	s_and_b64 s[40:41], s[42:43], s[40:41]
	s_nop 0
	v_cndmask_b32_e64 v56, v56, v34, s[40:41]
	v_cndmask_b32_e64 v57, v57, 14, s[40:41]
	v_cmp_ne_u32_e64 s[40:41], 15, v54
	s_and_b64 s[40:41], s[38:39], s[40:41]
	v_cmp_gt_f32_e64 s[38:39], v35, v56
	s_and_b64 s[38:39], s[40:41], s[38:39]
	s_nop 0
	v_cndmask_b32_e64 v56, v56, v35, s[38:39]
	v_cndmask_b32_e64 v57, v57, 15, s[38:39]
	v_cmp_ne_u32_e64 s[38:39], 16, v54
	s_and_b64 s[38:39], s[36:37], s[38:39]
	v_cmp_gt_f32_e64 s[36:37], v32, v56
	s_and_b64 s[36:37], s[38:39], s[36:37]
	s_nop 0
	v_cndmask_b32_e64 v56, v56, v32, s[36:37]
	v_cndmask_b32_e64 v57, v57, 16, s[36:37]
	v_cmp_ne_u32_e64 s[36:37], 17, v54
	s_and_b64 s[36:37], s[34:35], s[36:37]
	v_cmp_gt_f32_e64 s[34:35], v33, v56
	s_and_b64 s[34:35], s[36:37], s[34:35]
	s_nop 0
	v_cndmask_b32_e64 v56, v56, v33, s[34:35]
	v_cndmask_b32_e64 v57, v57, 17, s[34:35]
	v_cmp_ne_u32_e64 s[34:35], 18, v54
	s_and_b64 s[34:35], s[30:31], s[34:35]
	v_cmp_gt_f32_e64 s[30:31], v30, v56
	s_and_b64 s[30:31], s[34:35], s[30:31]
	s_nop 0
	v_cndmask_b32_e64 v56, v56, v30, s[30:31]
	v_cndmask_b32_e64 v57, v57, 18, s[30:31]
	v_cmp_ne_u32_e64 s[30:31], 19, v54
	s_and_b64 s[30:31], s[28:29], s[30:31]
	v_cmp_gt_f32_e64 s[28:29], v31, v56
	s_and_b64 s[28:29], s[30:31], s[28:29]
	s_nop 0
	v_cndmask_b32_e64 v56, v56, v31, s[28:29]
	v_cndmask_b32_e64 v57, v57, 19, s[28:29]
	v_cmp_ne_u32_e64 s[28:29], 20, v54
	s_and_b64 s[28:29], s[26:27], s[28:29]
	v_cmp_gt_f32_e64 s[26:27], v28, v56
	s_and_b64 s[26:27], s[28:29], s[26:27]
	s_nop 0
	v_cndmask_b32_e64 v56, v56, v28, s[26:27]
	v_cndmask_b32_e64 v57, v57, 20, s[26:27]
	v_cmp_ne_u32_e64 s[26:27], 21, v54
	s_and_b64 s[26:27], s[24:25], s[26:27]
	v_cmp_gt_f32_e64 s[24:25], v29, v56
	s_and_b64 s[24:25], s[26:27], s[24:25]
	s_nop 0
	v_cndmask_b32_e64 v56, v56, v29, s[24:25]
	v_cndmask_b32_e64 v57, v57, 21, s[24:25]
	v_cmp_ne_u32_e64 s[24:25], 22, v54
	s_and_b64 s[24:25], s[22:23], s[24:25]
	v_cmp_gt_f32_e64 s[22:23], v26, v56
	s_and_b64 s[22:23], s[24:25], s[22:23]
	s_nop 0
	v_cndmask_b32_e64 v56, v56, v26, s[22:23]
	v_cndmask_b32_e64 v57, v57, 22, s[22:23]
	v_cmp_ne_u32_e64 s[22:23], 23, v54
	s_and_b64 s[22:23], s[20:21], s[22:23]
	v_cmp_gt_f32_e64 s[20:21], v27, v56
	s_and_b64 s[20:21], s[22:23], s[20:21]
	s_nop 0
	v_cndmask_b32_e64 v56, v56, v27, s[20:21]
	v_cndmask_b32_e64 v57, v57, 23, s[20:21]
	v_cmp_ne_u32_e64 s[20:21], 24, v54
	s_and_b64 s[20:21], s[18:19], s[20:21]
	v_cmp_gt_f32_e64 s[18:19], v24, v56
	s_and_b64 s[18:19], s[20:21], s[18:19]
	s_nop 0
	v_cndmask_b32_e64 v56, v56, v24, s[18:19]
	v_cndmask_b32_e64 v57, v57, 24, s[18:19]
	v_cmp_ne_u32_e64 s[18:19], 25, v54
	s_and_b64 s[18:19], s[16:17], s[18:19]
	v_cmp_gt_f32_e64 s[16:17], v25, v56
	s_and_b64 s[16:17], s[18:19], s[16:17]
	s_nop 0
	v_cndmask_b32_e64 v56, v56, v25, s[16:17]
	v_cndmask_b32_e64 v57, v57, 25, s[16:17]
	v_cmp_ne_u32_e64 s[16:17], 26, v54
	s_and_b64 s[16:17], s[14:15], s[16:17]
	v_cmp_gt_f32_e64 s[14:15], v22, v56
	s_and_b64 s[14:15], s[16:17], s[14:15]
	s_nop 0
	v_cndmask_b32_e64 v56, v56, v22, s[14:15]
	v_cndmask_b32_e64 v57, v57, 26, s[14:15]
	v_cmp_ne_u32_e64 s[14:15], 27, v54
	s_and_b64 s[14:15], s[12:13], s[14:15]
	v_cmp_gt_f32_e64 s[12:13], v23, v56
	s_and_b64 s[12:13], s[14:15], s[12:13]
	s_nop 0
	v_cndmask_b32_e64 v56, v56, v23, s[12:13]
	v_cndmask_b32_e64 v57, v57, 27, s[12:13]
	v_cmp_ne_u32_e64 s[12:13], 28, v54
	s_and_b64 s[12:13], s[10:11], s[12:13]
	v_cmp_gt_f32_e64 s[10:11], v20, v56
	s_and_b64 s[10:11], s[12:13], s[10:11]
	s_nop 0
	v_cndmask_b32_e64 v56, v56, v20, s[10:11]
	v_cndmask_b32_e64 v57, v57, 28, s[10:11]
	v_cmp_ne_u32_e64 s[10:11], 29, v54
	s_and_b64 s[10:11], s[4:5], s[10:11]
	v_cmp_gt_f32_e64 s[4:5], v21, v56
	s_and_b64 s[4:5], s[10:11], s[4:5]
	s_nop 0
	v_cndmask_b32_e64 v56, v56, v21, s[4:5]
	v_cndmask_b32_e64 v57, v57, 29, s[4:5]
	v_cmp_ne_u32_e64 s[4:5], 30, v54
	s_and_b64 s[74:75], s[74:75], s[4:5]
	v_cmp_gt_f32_e64 s[4:5], v16, v56
	s_and_b64 s[4:5], s[74:75], s[4:5]
	s_nop 0
	v_cndmask_b32_e64 v56, v56, v16, s[4:5]
	v_cndmask_b32_e64 v57, v57, 30, s[4:5]
	v_cmp_ne_u32_e64 s[4:5], 31, v54
	s_and_b64 s[86:87], vcc, s[4:5]
	v_cmp_gt_f32_e32 vcc, v17, v56
	s_and_b64 vcc, s[86:87], vcc
	s_nop 0
	v_cndmask_b32_e32 v58, v56, v17, vcc
	v_cndmask_b32_e64 v56, v57, 31, vcc
	v_cmp_eq_u32_e32 vcc, 0, v56
	s_or_b64 vcc, s[0:1], vcc
	v_cmp_ne_u32_e64 s[4:5], 30, v56
	v_cndmask_b32_e32 v52, v52, v18, vcc
	v_cmp_ne_u32_e32 vcc, 1, v56
	s_and_b64 s[0:1], s[70:71], vcc
	v_cmp_gt_f32_e32 vcc, v53, v52
	s_and_b64 vcc, s[0:1], vcc
	s_nop 0
	v_cndmask_b32_e32 v52, v52, v53, vcc
	v_cndmask_b32_e64 v53, 0, 1, vcc
	v_cmp_ne_u32_e32 vcc, 2, v56
	s_and_b64 s[0:1], s[66:67], vcc
	v_cmp_gt_f32_e32 vcc, v50, v52
	s_and_b64 vcc, s[0:1], vcc
	s_nop 0
	v_cndmask_b32_e32 v50, v52, v50, vcc
	v_cndmask_b32_e64 v52, v53, 2, vcc
	v_cmp_ne_u32_e32 vcc, 3, v56
	s_and_b64 s[0:1], s[64:65], vcc
	v_cmp_gt_f32_e32 vcc, v51, v50
	s_and_b64 vcc, s[0:1], vcc
	s_nop 0
	v_cndmask_b32_e32 v50, v50, v51, vcc
	v_cndmask_b32_e64 v51, v52, 3, vcc
	v_cmp_ne_u32_e32 vcc, 4, v56
	s_and_b64 s[0:1], s[62:63], vcc
	v_cmp_gt_f32_e32 vcc, v48, v50
	s_and_b64 vcc, s[0:1], vcc
	s_nop 0
	v_cndmask_b32_e32 v48, v50, v48, vcc
	v_cndmask_b32_e64 v50, v51, 4, vcc
	v_cmp_ne_u32_e32 vcc, 5, v56
	s_and_b64 s[0:1], s[60:61], vcc
	v_cmp_gt_f32_e32 vcc, v49, v48
	s_and_b64 vcc, s[0:1], vcc
	s_nop 0
	v_cndmask_b32_e32 v48, v48, v49, vcc
	v_cndmask_b32_e64 v49, v50, 5, vcc
	v_cmp_ne_u32_e32 vcc, 6, v56
	s_and_b64 s[0:1], s[58:59], vcc
	v_cmp_gt_f32_e32 vcc, v46, v48
	s_and_b64 vcc, s[0:1], vcc
	s_nop 0
	v_cndmask_b32_e32 v46, v48, v46, vcc
	v_cndmask_b32_e64 v48, v49, 6, vcc
	v_cmp_ne_u32_e32 vcc, 7, v56
	s_and_b64 s[0:1], s[56:57], vcc
	v_cmp_gt_f32_e32 vcc, v47, v46
	s_and_b64 vcc, s[0:1], vcc
	s_nop 0
	v_cndmask_b32_e32 v46, v46, v47, vcc
	v_cndmask_b32_e64 v47, v48, 7, vcc
	v_cmp_ne_u32_e32 vcc, 8, v56
	s_and_b64 s[0:1], s[54:55], vcc
	v_cmp_gt_f32_e32 vcc, v44, v46
	s_and_b64 vcc, s[0:1], vcc
	s_nop 0
	v_cndmask_b32_e32 v44, v46, v44, vcc
	v_cndmask_b32_e64 v46, v47, 8, vcc
	v_cmp_ne_u32_e32 vcc, 9, v56
	s_and_b64 s[0:1], s[52:53], vcc
	v_cmp_gt_f32_e32 vcc, v45, v44
	s_and_b64 vcc, s[0:1], vcc
	s_nop 0
	v_cndmask_b32_e32 v44, v44, v45, vcc
	v_cndmask_b32_e64 v45, v46, 9, vcc
	v_cmp_ne_u32_e32 vcc, 10, v56
	s_and_b64 s[0:1], s[50:51], vcc
	v_cmp_gt_f32_e32 vcc, v42, v44
	s_and_b64 vcc, s[0:1], vcc
	s_nop 0
	v_cndmask_b32_e32 v42, v44, v42, vcc
	v_cndmask_b32_e64 v44, v45, 10, vcc
	v_cmp_ne_u32_e32 vcc, 11, v56
	s_and_b64 s[0:1], s[48:49], vcc
	v_cmp_gt_f32_e32 vcc, v43, v42
	s_and_b64 vcc, s[0:1], vcc
	s_nop 0
	v_cndmask_b32_e32 v42, v42, v43, vcc
	v_cndmask_b32_e64 v43, v44, 11, vcc
	v_cmp_ne_u32_e32 vcc, 12, v56
	s_and_b64 s[0:1], s[46:47], vcc
	v_cmp_gt_f32_e32 vcc, v40, v42
	s_and_b64 vcc, s[0:1], vcc
	s_nop 0
	v_cndmask_b32_e32 v40, v42, v40, vcc
	v_cndmask_b32_e64 v42, v43, 12, vcc
	v_cmp_ne_u32_e32 vcc, 13, v56
	s_and_b64 s[0:1], s[44:45], vcc
	v_cmp_gt_f32_e32 vcc, v41, v40
	s_and_b64 vcc, s[0:1], vcc
	s_nop 0
	v_cndmask_b32_e32 v40, v40, v41, vcc
	v_cndmask_b32_e64 v41, v42, 13, vcc
	v_cmp_ne_u32_e32 vcc, 14, v56
	s_and_b64 s[0:1], s[42:43], vcc
	v_cmp_gt_f32_e32 vcc, v34, v40
	s_and_b64 vcc, s[0:1], vcc
	s_nop 0
	v_cndmask_b32_e32 v34, v40, v34, vcc
	v_cndmask_b32_e64 v40, v41, 14, vcc
	v_cmp_ne_u32_e32 vcc, 15, v56
	s_and_b64 s[0:1], s[40:41], vcc
	v_cmp_gt_f32_e32 vcc, v35, v34
	s_and_b64 vcc, s[0:1], vcc
	s_nop 0
	v_cndmask_b32_e32 v34, v34, v35, vcc
	v_cndmask_b32_e64 v35, v40, 15, vcc
	v_cmp_ne_u32_e32 vcc, 16, v56
	s_and_b64 s[0:1], s[38:39], vcc
	v_cmp_gt_f32_e32 vcc, v32, v34
	s_and_b64 vcc, s[0:1], vcc
	s_nop 0
	v_cndmask_b32_e32 v32, v34, v32, vcc
	v_cndmask_b32_e64 v34, v35, 16, vcc
	v_cmp_ne_u32_e32 vcc, 17, v56
	s_and_b64 s[0:1], s[36:37], vcc
	v_cmp_gt_f32_e32 vcc, v33, v32
	s_and_b64 vcc, s[0:1], vcc
	s_nop 0
	v_cndmask_b32_e32 v32, v32, v33, vcc
	v_cndmask_b32_e64 v33, v34, 17, vcc
	v_cmp_ne_u32_e32 vcc, 18, v56
	s_and_b64 s[0:1], s[34:35], vcc
	v_cmp_gt_f32_e32 vcc, v30, v32
	s_and_b64 vcc, s[0:1], vcc
	s_nop 0
	v_cndmask_b32_e32 v30, v32, v30, vcc
	v_cndmask_b32_e64 v32, v33, 18, vcc
	v_cmp_ne_u32_e32 vcc, 19, v56
	s_and_b64 s[0:1], s[30:31], vcc
	v_cmp_gt_f32_e32 vcc, v31, v30
	s_and_b64 vcc, s[0:1], vcc
	s_nop 0
	v_cndmask_b32_e32 v30, v30, v31, vcc
	v_cndmask_b32_e64 v31, v32, 19, vcc
	v_cmp_ne_u32_e32 vcc, 20, v56
	s_and_b64 s[0:1], s[28:29], vcc
	v_cmp_gt_f32_e32 vcc, v28, v30
	s_and_b64 vcc, s[0:1], vcc
	s_nop 0
	v_cndmask_b32_e32 v28, v30, v28, vcc
	v_cndmask_b32_e64 v30, v31, 20, vcc
	v_cmp_ne_u32_e32 vcc, 21, v56
	s_and_b64 s[0:1], s[26:27], vcc
	v_cmp_gt_f32_e32 vcc, v29, v28
	s_and_b64 vcc, s[0:1], vcc
	s_nop 0
	v_cndmask_b32_e32 v28, v28, v29, vcc
	v_cndmask_b32_e64 v29, v30, 21, vcc
	v_cmp_ne_u32_e32 vcc, 22, v56
	s_and_b64 s[0:1], s[24:25], vcc
	v_cmp_gt_f32_e32 vcc, v26, v28
	s_and_b64 vcc, s[0:1], vcc
	s_nop 0
	v_cndmask_b32_e32 v26, v28, v26, vcc
	v_cndmask_b32_e64 v28, v29, 22, vcc
	v_cmp_ne_u32_e32 vcc, 23, v56
	s_and_b64 s[0:1], s[22:23], vcc
	v_cmp_gt_f32_e32 vcc, v27, v26
	s_and_b64 vcc, s[0:1], vcc
	s_nop 0
	v_cndmask_b32_e32 v26, v26, v27, vcc
	v_cndmask_b32_e64 v27, v28, 23, vcc
	v_cmp_ne_u32_e32 vcc, 24, v56
	s_and_b64 s[0:1], s[20:21], vcc
	v_cmp_gt_f32_e32 vcc, v24, v26
	s_and_b64 vcc, s[0:1], vcc
	s_nop 0
	v_cndmask_b32_e32 v24, v26, v24, vcc
	v_cndmask_b32_e64 v26, v27, 24, vcc
	v_cmp_ne_u32_e32 vcc, 25, v56
	s_and_b64 s[0:1], s[18:19], vcc
	v_cmp_gt_f32_e32 vcc, v25, v24
	s_and_b64 vcc, s[0:1], vcc
	s_nop 0
	v_cndmask_b32_e32 v24, v24, v25, vcc
	v_cndmask_b32_e64 v25, v26, 25, vcc
	v_cmp_ne_u32_e32 vcc, 26, v56
	s_and_b64 s[0:1], s[16:17], vcc
	v_cmp_gt_f32_e32 vcc, v22, v24
	s_and_b64 vcc, s[0:1], vcc
	s_nop 0
	v_cndmask_b32_e32 v22, v24, v22, vcc
	v_cndmask_b32_e64 v24, v25, 26, vcc
	v_cmp_ne_u32_e32 vcc, 27, v56
	s_and_b64 s[0:1], s[14:15], vcc
	v_cmp_gt_f32_e32 vcc, v23, v22
	s_and_b64 vcc, s[0:1], vcc
	s_nop 0
	v_cndmask_b32_e32 v22, v22, v23, vcc
	v_cndmask_b32_e64 v23, v24, 27, vcc
	v_cmp_ne_u32_e32 vcc, 28, v56
	s_and_b64 s[0:1], s[12:13], vcc
	v_cmp_gt_f32_e32 vcc, v20, v22
	s_and_b64 vcc, s[0:1], vcc
	v_cmp_ne_u32_e64 s[0:1], 29, v56
	v_cndmask_b32_e32 v20, v22, v20, vcc
	s_and_b64 s[2:3], s[10:11], s[0:1]
	v_cmp_gt_f32_e64 s[0:1], v21, v20
	s_and_b64 s[0:1], s[2:3], s[0:1]
	s_and_b64 s[2:3], s[74:75], s[4:5]
	v_cndmask_b32_e64 v20, v20, v21, s[0:1]
	v_cmp_gt_f32_e64 s[4:5], v16, v20
	s_and_b64 s[4:5], s[2:3], s[4:5]
	v_cmp_ne_u32_e64 s[10:11], 31, v56
	v_cndmask_b32_e64 v16, v20, v16, s[4:5]
	s_and_b64 s[2:3], s[86:87], s[10:11]
	v_cmp_gt_f32_e64 s[10:11], v17, v16
	s_and_b64 s[10:11], s[2:3], s[10:11]
	s_mov_b32 s74, 0x3c800000
	v_cndmask_b32_e64 v20, v16, v17, s[10:11]
	v_exp_f32_e32 v16, v1
	v_sub_f32_e32 v1, v58, v55
	v_mul_f32_e32 v1, 0x3fb8aa3b, v1
	v_exp_f32_e32 v17, v1
	v_sub_f32_e32 v1, v20, v55
	v_mul_f32_e32 v1, 0x3fb8aa3b, v1
	v_exp_f32_e32 v1, v1
	v_add_f32_e32 v21, 1.0, v16
	v_add_f32_e32 v21, v21, v17
	v_cndmask_b32_e64 v20, v23, 28, vcc
	v_add_f32_e32 v23, v21, v1
	v_div_scale_f32 v21, s[2:3], v23, v23, 1.0
	v_rcp_f32_e32 v27, v21
	v_cndmask_b32_e64 v20, v20, 29, s[0:1]
	v_cndmask_b32_e64 v20, v20, 30, s[4:5]
	v_cndmask_b32_e64 v24, v20, 31, s[10:11]
	v_fma_f32 v20, -v21, v27, 1.0
	v_fmac_f32_e32 v27, v20, v27
	v_div_scale_f32 v20, vcc, 1.0, v23, 1.0
	v_mul_f32_e32 v28, v20, v27
	v_fma_f32 v22, -v21, v28, v20
	v_fmac_f32_e32 v28, v22, v27
	s_add_i32 s0, 0, 0x22500
	v_fma_f32 v20, -v21, v28, v20
	v_lshl_add_u32 v21, v2, 2, s0
	ds_add_rtn_u32 v21, v21, v219
	v_lshl_add_u32 v22, v54, 2, s0
	ds_add_rtn_u32 v22, v22, v219
	v_lshl_add_u32 v25, v56, 2, s0
	ds_add_rtn_u32 v26, v25, v219
	v_lshl_add_u32 v25, v24, 2, s0
	ds_add_rtn_u32 v25, v25, v219
	v_div_fmas_f32 v20, v20, v27, v28
	v_div_fixup_f32 v20, v20, v23, 1.0
	s_mov_b64 s[86:87], 0x80
	s_waitcnt lgkmcnt(3)
	v_pk_mul_f32 v[16:17], v[16:17], v[20:21] op_sel_hi:[1,0]
	v_mul_f32_e32 v23, v1, v20
